# hand-written weight-conversion loop (k-paired LDS layout, double-buffered LDS, one barrier per half, early prefetch) + split rebalanced to 160 mixer / 96 converter workgroups
# speedup vs baseline: 1.0073x; 1.0043x over previous
; #define LAS __attribute__((address_space(3)))
; __device__ __forceinline__ unsigned xb_add(unsigned* p, unsigned v) { return __hip_atomic_fetch_add(p, v, __ATOMIC_RELAXED, __HIP_MEMORY_SCOPE_AGENT); }
; __device__ __forceinline__ unsigned xb_xcc_id() { return (unsigned)__builtin_amdgcn_s_getreg((3 << 11) | 20) & 0xFu; }
; __device__ __forceinline__ XcdBarrier xcd_barrier_post(unsigned* bar, volatile LAS unsigned* st, unsigned gsz) {
;     XcdBarrier b; b.bar = bar; b.x = xb_xcc_id(); b.st = st; b.gsz = gsz;
;     if (threadIdx.x == 0) (void)xb_add(&bar[XB_XCNT(b.x)], 1u);
;     return b;
; __global__ void __launch_bounds__(512, 2) mk_fwd(Params p) {
;     ...
;     const int lo = p.ph_lo, hi = p.ph_hi;
;     XcdBarrier bar; bar.bar = (unsigned*)(p.ws + WS_CTL); bar.x = 0; bar.st = misc + 8; bar.gsz = (unsigned)G;
;     if (hi - lo > 1) bar = xcd_barrier_post((unsigned*)(p.ws + WS_CTL), misc + 8, (unsigned)G);
;     const bool split_ok = (G == 256) && (hi - lo > 1);
;     XcdBarrier bar2; bar2.bar = (unsigned*)(p.ws + WS_CTL) + 4096; bar2.x = 0; bar2.st = misc + 12; bar2.gsz = (unsigned)MIX_GW;
;     if (split_ok && bx < MIX_GW) bar2 = xcd_barrier_post((unsigned*)(p.ws + WS_CTL) + 4096, misc + 12, (unsigned)MIX_GW);
.LBB0_7:
	s_cmpk_lg_i32 s58, 0x100
	s_cselect_b64 s[14:15], -1, 0
	s_cmpk_eq_i32 s58, 0x100
	s_load_dwordx16 s[60:75], s[0:1], 0x0
	s_load_dwordx16 s[36:51], s[0:1], 0x40
	s_cselect_b64 s[0:1], -1, 0
	s_and_b64 s[0:1], s[10:11], s[0:1]
	s_add_u32 s8, s26, 0x4000
	s_addc_u32 s9, s27, 0
	s_cmpk_lt_i32 s2, 0xa0
	s_cselect_b64 s[16:17], -1, 0
	v_writelane_b32 v249, s0, 10
	s_nop 1
	v_writelane_b32 v249, s1, 11
	s_and_b64 s[0:1], s[16:17], s[0:1]
	s_andn2_b64 vcc, exec, s[0:1]
	s_cbranch_vccnz .LBB0_12
	s_getreg_b32 s0, hwreg(HW_REG_XCC_ID, 0, 4)
	s_and_b32 s97, s0, 15
	v_cmp_eq_u32_e32 vcc, 0, v0
	s_and_saveexec_b64 s[0:1], vcc
	s_cbranch_execz .LBB0_11
	s_mov_b64 s[4:5], exec
	v_mbcnt_lo_u32_b32 v1, s4, 0
	v_mbcnt_hi_u32_b32 v1, s5, v1
	v_cmp_eq_u32_e32 vcc, 0, v1
	s_and_b64 s[6:7], exec, vcc
	s_mov_b64 exec, s[6:7]
	s_cbranch_execz .LBB0_11
	s_lshl_b32 s6, s97, 8
	s_bcnt1_i32_b64 s4, s[4:5]
	v_mov_b32_e32 v1, s6
	v_mov_b32_e32 v2, s4
	global_atomic_add v1, v2, s[8:9] offset:1024

; #define REP(k) _Pragma("unroll") for (int rep_ = 0; rep_ < 1 + (int)(((REP_MASK) >> (k)) & 1u); ++rep_)
; __global__ void __launch_bounds__(512, 2) mk_fwd(Params p) {
;     ...
;     for (int l = 0; l < 2; ++l) {
;         const int pb = 1 + 10 * l;
;         const char* H = (const char*)(p.ws + WS_H);
;         if (EN(3) && IN(pb + 0)) REP(3) { if (G == 256 && !split_ok && bx < 4) ph_rbias(p, l, bx); if (l == 0) ph_norm1_l0(p); else ph_norm1(p, 1, lds); }
;         SEAM(pb + 0);
;         const bool split = split_ok && l == 0 && EN(2);
;         const int vG = split ? MIX_GW : G;
;         if (EN(4) && IN(pb + 1) && (!split || bx < MIX_GW)) REP(4) {
;             SchedProj S{H, (const char*)(p.ws + WS_WIN) + (size_t)l * NPROJ * 2048 * 2, (const char*)(p.ws + WS_WPQ) + (size_t)l * 512 * 2048 * 2, vG, bx};
;             EpiProj E{(bf16_t*)(p.ws + WS_PROJ), (bf16_t*)(p.ws + WS_PQT), (const float*)(p.ws + WS_ROPE), (const float*)(p.ws + WS_ROPE) + NT * 8};
;             pg8::gemm_phase<EpiProj, SchedProj>(lds, 2048, 2048, 2048, S, E);
;         }
;         if (split) { if (bx < MIX_GW && IN(pb + 1) && IN(pb + 2)) xcd_barrier(bar2); } else SEAM(pb + 1);
;         if (IN(pb + 2)) {
;             if (!split || bx < MIX_GW) {
;                 if (EN(5)) REP(5) ph_fft(p, lds, bx, vG);
;                 __syncthreads();
;                 if (EN(8)) REP(8) ph_mixers(p, l, lds, bx, vG);
;             } else { if (bx - MIX_GW < 4) ph_rbias(p, 0, bx - MIX_GW); ph_weights(p, lds, 240, 6880, bx - MIX_GW, G - MIX_GW); }
;         }
;         SEAM(pb + 2);
;         if (EN(9) && IN(pb + 3)) REP(9) { ph_merge(p, l, lds); }
;         SEAM(pb + 3);
;         if (EN(10) && IN(pb + 4)) REP(10) {
;             SchedDense S{(const char*)(p.ws + WS_YN), (const char*)(p.ws + WS_WOUT) + (size_t)l * 2048 * 2048 * 2, 32, 8, 2048, G, bx};
;             const float* modl = (const float*)(p.ws + WS_MOD) + (size_t)l * 4 * 12288;
;             if (G == 256) {
;                 float* xch = (float*)(p.ws + WS_XE + (size_t)l * 8 * MiB);
;                 EpiWoutN E{l == 0 ? p.in[0] : nullptr, (const bf16_t*)(p.ws + WS_X), (bf16_t*)(p.ws + WS_X2), modl + 2 * 2048, p.in[14] + (size_t)l * DM, modl + 3 * 2048,
;                            (const bf16_t*)(p.ws + WS_WRT) + (size_t)l * 16 * 2048, (bf16_t*)(p.ws + WS_H), (float*)(p.ws + WS_AFF), (const float*)(p.ws + WS_XE + 16 * MiB) + (size_t)l * 64,
.LBB0_329:
	s_ashr_i32 s0, s2, 31
	v_writelane_b32 v249, s0, 51
	s_lshr_b32 s0, s0, 29
	s_add_i32 s0, s2, s0
	s_add_i32 s12, s2, 0x70
	s_and_b32 s1, s0, -8
	s_lshl_b32 s4, s12, 1
	s_sub_i32 s1, s2, s1
	s_add_i32 s5, s4, 0xffffe520
	s_cmpk_gt_u32 s2, 0xcff
	s_cselect_b32 s21, 16, 0
	s_cselect_b32 s18, 0x800, 0
	s_cselect_b32 s13, 0xd00, 0
	s_cselect_b32 s20, 0x8000, 0
	s_cmpk_lt_u32 s2, 0xd00
	s_cselect_b32 s31, s4, s5
	s_or_b32 s5, s4, 1
	s_addk_i32 s4, 0xe521
	s_lshl_b32 s6, s1, 5
	s_cmp_lt_i32 s1, 0
	s_mul_i32 s7, s1, 33
	s_cselect_b32 s22, 53, 52
	s_cselect_b32 s3, s7, s6
	s_cmpk_lt_u32 s2, 0xd00
	s_cselect_b32 s19, s5, s4
	s_cmpk_gt_u32 s2, 0xcff
	s_cselect_b32 s23, 0x200000, 0
	s_add_u32 s16, s26, 0x24400000
	s_addc_u32 s17, s27, 0
	s_cmpk_lg_i32 s58, 0x100
	s_cselect_b64 s[4:5], -1, 0
	s_cmp_gt_i32 s2, 3
	s_cselect_b64 s[6:7], -1, 0
	s_or_b64 s[4:5], s[6:7], s[4:5]
	v_writelane_b32 v249, s3, 52
	s_nor_b64 s[4:5], s[10:11], s[4:5]
	v_writelane_b32 v249, s4, 53
	s_mul_i32 s1, s22, s1
	s_mov_b32 s61, 0
	v_writelane_b32 v249, s5, 54
	s_add_u32 s4, s26, 0x3b380000
	s_addc_u32 s5, s27, 0
	s_add_u32 s7, s26, 0x32300000
	v_writelane_b32 v249, s4, 55
	s_addc_u32 s43, s27, 0
	v_mov_b32_e32 v1, 0x12e0
	v_writelane_b32 v249, s5, 56
	s_add_u32 s4, s26, 0x100000
	s_addc_u32 s5, s27, 0
	s_lshl_b32 s3, s2, 5
	s_add_u32 s62, s26, 0x37300000
	v_writelane_b32 v249, s4, 57
	s_addc_u32 s63, s27, 0
	s_mov_b64 s[52:53], s[72:73]
	v_writelane_b32 v249, s5, 58
	s_add_u32 s4, s26, 0x31220000
	v_writelane_b32 v249, s3, 59
	s_addc_u32 s5, s27, 0
	v_writelane_b32 v249, s4, 60
	v_mov_b32_e32 v195, 0
	v_mov_b32_e32 v217, 0x358637bd
	v_writelane_b32 v249, s5, 61
	s_add_u32 s4, s26, 0x20400000
	s_addc_u32 s5, s27, 0
	v_writelane_b32 v249, s4, 62
	v_mov_b32_e32 v219, 0x260
	v_mov_b32_e32 v221, 1
	v_writelane_b32 v249, s5, 63
	s_add_u32 s4, s26, 0x1c400000
	s_addc_u32 s5, s27, 0
	v_writelane_b32 v250, s4, 0
	v_readlane_b32 vcc_lo, v249, 47
	v_readlane_b32 vcc_hi, v249, 48
	v_writelane_b32 v250, s5, 1
	s_add_u32 s4, s70, 0x2000
	s_addc_u32 s5, s71, 0
	s_lshl_b32 s3, s58, 5
	s_add_u32 s54, s26, 0x1000
	v_writelane_b32 v250, s4, 2
	s_addc_u32 s55, s27, 0
	v_readlane_b32 s80, v249, 0
	v_writelane_b32 v250, s5, 3
	s_add_u32 s4, s26, 0x1100
	v_writelane_b32 v250, s3, 4
	s_addc_u32 s5, s27, 0
	v_writelane_b32 v250, s4, 5
	v_readlane_b32 s84, v249, 4
	v_readlane_b32 s85, v249, 5
	v_writelane_b32 v250, s5, 6
	s_add_u32 s4, s26, 0x1200
	s_addc_u32 s5, s27, 0
	v_writelane_b32 v250, s4, 7
	v_readlane_b32 s81, v249, 1
	v_readlane_b32 s82, v249, 2
	v_writelane_b32 v250, s5, 8
	s_add_u32 s4, s26, 0x1300
	s_addc_u32 s5, s27, 0
	v_writelane_b32 v250, s4, 9
	s_cmp_eq_u32 s96, 15
	v_readlane_b32 s83, v249, 3
	v_writelane_b32 v250, s5, 10
	s_cselect_b64 s[4:5], -1, 0
	v_writelane_b32 v250, s4, 11
	s_cmp_eq_u32 s96, 14
	v_readlane_b32 s64, v249, 29
	v_writelane_b32 v250, s5, 12
	s_cselect_b64 s[4:5], -1, 0
	v_writelane_b32 v250, s4, 13
	s_cmp_eq_u32 s96, 13
	v_readlane_b32 s74, v249, 39
	v_writelane_b32 v250, s5, 14
	s_cselect_b64 s[4:5], -1, 0
	v_writelane_b32 v250, s4, 15
	s_cmp_eq_u32 s96, 12
	v_readlane_b32 s75, v249, 40
	v_writelane_b32 v250, s5, 16
	s_cselect_b64 s[4:5], -1, 0
	v_writelane_b32 v250, s4, 17
	s_cmp_eq_u32 s96, 11
	v_readlane_b32 s72, v249, 37
	v_writelane_b32 v250, s5, 18
	s_cselect_b64 s[4:5], -1, 0
	v_writelane_b32 v250, s4, 19
	s_cmp_eq_u32 s96, 10
	v_readlane_b32 s73, v249, 38
	v_writelane_b32 v250, s5, 20
	s_cselect_b64 s[4:5], -1, 0
	v_writelane_b32 v250, s4, 21
	s_cmp_eq_u32 s96, 9
	v_readlane_b32 s79, v249, 44
	v_writelane_b32 v250, s5, 22
	s_cselect_b64 s[4:5], -1, 0
	v_writelane_b32 v250, s4, 23
	s_cmp_eq_u32 s96, 8
	v_readlane_b32 s70, v249, 35
	v_writelane_b32 v250, s5, 24
	s_cselect_b64 s[4:5], -1, 0
	v_writelane_b32 v250, s4, 25
	s_cmp_eq_u32 s96, 7
	v_readlane_b32 s71, v249, 36
	v_writelane_b32 v250, s5, 26
	s_cselect_b64 s[4:5], -1, 0
	v_writelane_b32 v250, s4, 27
	s_cmp_eq_u32 s96, 6
	v_readlane_b32 s76, v249, 41
	v_writelane_b32 v250, s5, 28
	s_cselect_b64 s[4:5], -1, 0
	v_writelane_b32 v250, s4, 29
	s_cmp_eq_u32 s96, 5
	v_readlane_b32 s77, v249, 42
	v_writelane_b32 v250, s5, 30
	s_cselect_b64 s[4:5], -1, 0
	v_writelane_b32 v250, s4, 31
	s_cmp_eq_u32 s96, 4
	v_readlane_b32 s65, v249, 30
	v_writelane_b32 v250, s5, 32
	s_cselect_b64 s[4:5], -1, 0
	v_writelane_b32 v250, s4, 33
	s_cmp_eq_u32 s96, 3
	v_readlane_b32 s69, v249, 34
	v_writelane_b32 v250, s5, 34
	s_cselect_b64 s[4:5], -1, 0
	v_writelane_b32 v250, s4, 35
	s_cmp_eq_u32 s96, 2
	v_readlane_b32 s78, v249, 43
	v_writelane_b32 v250, s5, 36
	s_cselect_b64 s[4:5], -1, 0
	v_writelane_b32 v250, s4, 37
	s_cmp_eq_u32 s96, 1
	v_readlane_b32 s68, v249, 33
	v_writelane_b32 v250, s5, 38
	s_cselect_b64 s[4:5], -1, 0
	v_writelane_b32 v250, s4, 39
	s_cmp_eq_u32 s96, 0
	v_readlane_b32 s66, v249, 31
	v_writelane_b32 v250, s5, 40
	s_cselect_b64 s[4:5], -1, 0
	v_writelane_b32 v250, s4, 41
	v_readlane_b32 s67, v249, 32
	v_readlane_b32 s86, v249, 6
	v_writelane_b32 v250, s5, 42
	s_lshl_b32 s4, s96, 8
	s_add_u32 s4, s26, s4
	s_addc_u32 s5, s27, 0
	s_add_u32 s10, s4, 0x1400
	s_addc_u32 s11, s5, 0
	v_writelane_b32 v250, s10, 43
	s_add_u32 s4, s4, 0x2400
	s_addc_u32 s5, s5, 0
	v_writelane_b32 v250, s11, 44
	v_writelane_b32 v250, s4, 45
	v_readlane_b32 s87, v249, 7
	v_mov_b32_e32 v248, -1
	v_writelane_b32 v250, s5, 46
	s_add_u32 s4, s26, 0x3400
	s_addc_u32 s5, s27, 0
	s_add_u32 s14, s26, 0x1200000
	s_addc_u32 s15, s27, 0
	s_add_u32 s38, s26, 0x2c00000
	v_writelane_b32 v250, s4, 47
	s_addc_u32 s39, s27, 0
	v_mov_b32_e32 v218, 0xf149f2ca
	v_writelane_b32 v250, s5, 48
	s_add_u32 s4, s26, 0x26400000
	s_addc_u32 s5, s27, 0
;     __device__ __forceinline__ bool next(int i, GUnit& u) const {
;         const int L = i * G + c; if (L >= 480) return false;
;         if (L < 416) { int pm, pn; pg8::dense_map(L, 32, 13, pm, pn); u.pm = pm; u.pn = pn; u.z = 0; u.a = H + (size_t)pm * 256 * 2048 * 2; u.b = WIN + (size_t)pn * 256 * 2048 * 2; }
;         else { int pm, pn; pg8::dense_map(L - 416, 2, 32, pm, pn); u.pm = pm; u.pn = pn + 64; u.z = 0; u.a = WPQ + (size_t)pm * 256 * 2048 * 2; u.b = H + (size_t)pn * 256 * 2048 * 2; }
;         return true;
;     }
	v_writelane_b32 v250, s4, 49
	s_add_u32 s3, s26, 0x29800000
	v_mov_b32_e32 v227, 0x7f800000
	v_writelane_b32 v250, s5, 50
	v_writelane_b32 v250, s3, 51
	s_addc_u32 s3, s27, 0
	s_add_u32 s4, s26, 0x180000
	s_addc_u32 s5, s27, 0
	v_writelane_b32 v250, s4, 52
	s_nop 1
	v_writelane_b32 v250, s5, 53
	s_add_u32 s4, s26, 0x1c0000
	s_addc_u32 s5, s27, 0
	v_writelane_b32 v250, s4, 54
	s_cmpk_lt_i32 s2, 0x1e0
	s_nop 0
	v_writelane_b32 v250, s5, 55
	s_cselect_b64 s[4:5], -1, 0
	v_writelane_b32 v250, s4, 56
	s_nop 1
	v_writelane_b32 v250, s5, 57
	s_add_i32 s5, s2, 0x60
	s_lshl_b32 s4, s2, 3
	s_lshr_b32 s10, s5, 3
	s_and_b32 s4, s4, 56
	s_and_b32 s10, s10, 30
	s_add_i32 s10, s10, s4
	s_bfe_u32 s5, s5, 0x10003
	s_lshr_b32 s4, s10, 1
	v_writelane_b32 v250, s5, 58
	s_or_b32 s2, s4, 64
	v_writelane_b32 v250, s2, 59
	s_lshl_b32 s4, s10, 19
	s_lshl_b32 s2, s5, 20
	v_writelane_b32 v250, s2, 61
	s_add_u32 s2, s16, s4
	v_writelane_b32 v250, s2, 62
	s_addc_u32 s2, s17, 0
	s_ashr_i32 s42, s0, 3
	s_add_i32 s1, s1, s42
	s_mul_hi_i32 s0, s1, 0x4ec4ec4f
	s_lshr_b32 s4, s0, 31
	s_ashr_i32 s0, s0, 5
	s_add_i32 s0, s0, s4
	s_mul_i32 s4, s0, 0x68
	s_sub_i32 s1, s1, s4
	s_bfe_i32 s4, s1, 0x80000
	s_bfe_u32 s4, s4, 0x3000c
	s_add_i32 s4, s1, s4
	s_and_b32 s5, s4, 0xf8
	s_sub_i32 s1, s1, s5
	s_lshl_b32 s0, s0, 3
	s_bfe_i32 s4, s4, 0x80000
	s_sext_i32_i8 s1, s1
	s_sext_i32_i16 s10, s4
	s_add_i32 s4, s0, s1
	s_ashr_i32 s5, s4, 31
	s_ashr_i32 s0, s10, 3
	s_lshr_b32 s10, s10, 3
	s_lshl_b64 s[34:35], s[4:5], 20
	v_writelane_b32 v251, s0, 0
	s_add_u32 s0, s16, s34
	v_writelane_b32 v251, s0, 2
	s_addc_u32 s0, s17, s35
	s_bfe_i64 s[10:11], s[10:11], 0x100000
	v_writelane_b32 v251, s0, 3
	s_lshl_b64 s[0:1], s[10:11], 20
	v_writelane_b32 v251, s0, 4
	v_writelane_b32 v250, s2, 63
	s_nop 0
	v_writelane_b32 v251, s1, 5
	v_readlane_b32 s0, v249, 8
	v_readlane_b32 s1, v249, 9
	s_cmp_lt_i32 s0, 4
	s_cselect_b64 s[10:11], -1, 0
	s_cmp_gt_i32 s1, 3
	s_cselect_b64 s[34:35], -1, 0
	s_and_b64 s[10:11], s[10:11], s[34:35]
	s_and_b64 s[0:1], vcc, s[10:11]
	v_writelane_b32 v251, s0, 6
	s_nop 1
	v_writelane_b32 v251, s1, 7
	s_add_u32 s0, s26, 0x4200
	s_addc_u32 s1, s27, 0
	v_writelane_b32 v251, s0, 8
	s_nop 1
	v_writelane_b32 v251, s1, 9
	s_add_u32 s0, s26, 0x4400
	s_addc_u32 s1, s27, 0
	v_writelane_b32 v251, s0, 10
	s_nop 1
	v_writelane_b32 v251, s1, 11
	s_add_u32 s0, s26, 0x4500
	s_addc_u32 s1, s27, 0
	v_writelane_b32 v251, s0, 12
	s_nop 1
	v_writelane_b32 v251, s1, 13
	s_add_u32 s0, s26, 0x4600
	s_addc_u32 s1, s27, 0
	v_writelane_b32 v251, s0, 14
	s_nop 1
	v_writelane_b32 v251, s1, 15
	s_add_u32 s0, s26, 0x4700
	s_addc_u32 s1, s27, 0
	v_writelane_b32 v251, s0, 16
	s_nop 1
	v_writelane_b32 v251, s1, 17
	s_add_u32 s0, s26, 0x4800
	s_addc_u32 s1, s27, 0
	v_writelane_b32 v251, s0, 18
	s_nop 1
	v_writelane_b32 v251, s1, 19
	s_add_u32 s0, s26, 0x4900
	s_addc_u32 s1, s27, 0
	v_writelane_b32 v251, s0, 20
	s_nop 1
	v_writelane_b32 v251, s1, 21
	s_add_u32 s0, s26, 0x4a00
	s_addc_u32 s1, s27, 0
	v_writelane_b32 v251, s0, 22
	s_nop 1
	v_writelane_b32 v251, s1, 23
	s_add_u32 s0, s26, 0x4b00
	s_addc_u32 s1, s27, 0
	v_writelane_b32 v251, s0, 24
	s_nop 1
	v_writelane_b32 v251, s1, 25
	s_add_u32 s0, s26, 0x4c00
	s_addc_u32 s1, s27, 0
	v_writelane_b32 v251, s0, 26
	s_nop 1
	v_writelane_b32 v251, s1, 27
	s_add_u32 s0, s26, 0x4d00
	s_addc_u32 s1, s27, 0
	v_writelane_b32 v251, s0, 28
	s_nop 1
	v_writelane_b32 v251, s1, 29
	s_add_u32 s0, s26, 0x4e00
	s_addc_u32 s1, s27, 0
	v_writelane_b32 v251, s0, 30
	s_nop 1
	v_writelane_b32 v251, s1, 31
	s_add_u32 s0, s26, 0x4f00
	s_addc_u32 s1, s27, 0
	v_writelane_b32 v251, s0, 32
	s_nop 1
	v_writelane_b32 v251, s1, 33
	s_add_u32 s0, s26, 0x5000
	s_addc_u32 s1, s27, 0
	v_writelane_b32 v251, s0, 34
	s_nop 1
	v_writelane_b32 v251, s1, 35
	s_add_u32 s0, s26, 0x5100
	s_addc_u32 s1, s27, 0
	v_writelane_b32 v251, s0, 36
	s_nop 1
	v_writelane_b32 v251, s1, 37
	s_add_u32 s0, s26, 0x5200
	s_addc_u32 s1, s27, 0
	v_writelane_b32 v251, s0, 38
	s_nop 1
	v_writelane_b32 v251, s1, 39
	s_add_u32 s0, s26, 0x5300
	s_addc_u32 s1, s27, 0
	v_writelane_b32 v251, s0, 40
	s_cmp_eq_u32 s97, 15
	s_nop 0
	v_writelane_b32 v251, s1, 41
	s_cselect_b64 s[0:1], -1, 0
	v_writelane_b32 v251, s0, 42
	s_cmp_eq_u32 s97, 14
	s_nop 0
	v_writelane_b32 v251, s1, 43
	s_cselect_b64 s[0:1], -1, 0
	v_writelane_b32 v251, s0, 44
	s_cmp_eq_u32 s97, 13
	s_nop 0
	v_writelane_b32 v251, s1, 45
	s_cselect_b64 s[0:1], -1, 0
	v_writelane_b32 v251, s0, 46
	s_cmp_eq_u32 s97, 12
	s_nop 0
	v_writelane_b32 v251, s1, 47
	s_cselect_b64 s[0:1], -1, 0
	v_writelane_b32 v251, s0, 48
	s_cmp_eq_u32 s97, 11
	s_nop 0
	v_writelane_b32 v251, s1, 49
	s_cselect_b64 s[0:1], -1, 0
	v_writelane_b32 v251, s0, 50
	s_cmp_eq_u32 s97, 10
	s_nop 0
	v_writelane_b32 v251, s1, 51
	s_cselect_b64 s[0:1], -1, 0
	v_writelane_b32 v251, s0, 52
	s_cmp_eq_u32 s97, 9
	s_nop 0
	v_writelane_b32 v251, s1, 53
	s_cselect_b64 s[0:1], -1, 0
	v_writelane_b32 v251, s0, 54
	s_cmp_eq_u32 s97, 8
	s_nop 0
	v_writelane_b32 v251, s1, 55
	s_cselect_b64 s[0:1], -1, 0
	v_writelane_b32 v251, s0, 56
	s_cmp_eq_u32 s97, 7
	s_nop 0
	v_writelane_b32 v251, s1, 57
	s_cselect_b64 s[0:1], -1, 0
	v_writelane_b32 v251, s0, 58
	s_cmp_eq_u32 s97, 6
	s_nop 0
	v_writelane_b32 v251, s1, 59
	s_cselect_b64 s[0:1], -1, 0
	v_writelane_b32 v251, s0, 60
	s_cmp_eq_u32 s97, 5
	s_nop 0
	v_writelane_b32 v251, s1, 61
	s_cselect_b64 s[0:1], -1, 0
	v_writelane_b32 v251, s0, 62
	s_cmp_eq_u32 s97, 4
	s_nop 0
	v_writelane_b32 v251, s1, 63
	s_cselect_b64 s[0:1], -1, 0
	v_writelane_b32 v252, s0, 0
	s_cmp_eq_u32 s97, 3
	s_nop 0
	v_writelane_b32 v252, s1, 1
	s_cselect_b64 s[0:1], -1, 0
	v_writelane_b32 v252, s0, 2
; __device__ __forceinline__ bool tdecode(const Params& p, int it, TDesc& d) {
;     if (it >= 2 * 6880) return false;
;     const int l = it / 6880; int r = it % 6880;
;     d.ksc = nullptr;
;     if (r < 480) { const int kt = r / 30, nt = r % 30;
;         d.src = p.in[6] + ((size_t)l * 2048 + kt * 128) * DIN + nt * 128; d.lds_ = DIN;
;         d.dst = (nt < 4 ? (bf16_t*)(p.ws + WS_WPQ) + ((size_t)l * 512 + nt * 128) * 2048 : (bf16_t*)(p.ws + WS_WIN) + ((size_t)l * NPROJ + (nt - 4) * 128) * 2048) + kt * 128; d.ldd = 2048; return true; }
;     r -= 480;
;     if (r < 256) { const int kt = r / 16, nt = r % 16;
;         d.src = p.in[13] + ((size_t)l * 2048 + kt * 128) * 2048 + nt * 128; d.lds_ = 2048; d.ksc = p.in[12] + (size_t)l * 2048 + kt * 128;
;         d.dst = (bf16_t*)(p.ws + WS_WOUT) + ((size_t)l * 2048 + nt * 128) * 2048 + kt * 128; d.ldd = 2048; return true; }
;     r -= 256;
;     if (r < 4096) { const int isup = r / 2048, r2 = r % 2048, e = r2 / 128, kt = (r2 % 128) / 8, nt = r2 % 8;
;         d.src = p.in[isup ? 17 : 16] + (((size_t)l * 16 + e) * 2048 + kt * 128) * 1024 + nt * 128; d.lds_ = 1024;
;         d.dst = (bf16_t*)(p.ws + WS_WGU) + (((size_t)l * 16 + e) * 2048 + nt * 256 + isup * 128) * 2048 + kt * 128; d.ldd = 2048; return true; }
;     r -= 4096;
;     { const int e = r / 128, kt = (r % 128) / 16, nt = r % 16;
;         d.src = p.in[18] + (((size_t)l * 16 + e) * 1024 + kt * 128) * 2048 + nt * 128; d.lds_ = 2048;
;         d.dst = (bf16_t*)(p.ws + WS_WD) + (((size_t)l * 16 + e) * 2048 + nt * 128) * 1024 + kt * 128; d.ldd = 1024; return true; }
; }
; __global__ void __launch_bounds__(512, 2) mk_fwd(Params p) {
;     ...
;             } else { if (bx - MIX_GW < 4) ph_rbias(p, 0, bx - MIX_GW); ph_weights(p, lds, 240, 6880, bx - MIX_GW, G - MIX_GW); }
	s_cmp_eq_u32 s97, 2
	s_nop 0
	v_writelane_b32 v252, s1, 3
	s_cselect_b64 s[0:1], -1, 0
	v_writelane_b32 v252, s0, 4
	s_cmp_eq_u32 s97, 1
	s_nop 0
	v_writelane_b32 v252, s1, 5
	s_cselect_b64 s[0:1], -1, 0
	v_writelane_b32 v252, s0, 6
	s_cmp_eq_u32 s97, 0
	s_nop 0
	v_writelane_b32 v252, s1, 7
	s_cselect_b64 s[0:1], -1, 0
	v_writelane_b32 v252, s0, 8
	s_nop 1
	v_writelane_b32 v252, s1, 9
	s_lshl_b32 s0, s97, 8
	s_add_u32 s0, s8, s0
	s_addc_u32 s1, s9, 0
	s_add_u32 s8, s0, 0x1400
	s_addc_u32 s9, s1, 0
	v_writelane_b32 v252, s8, 10
	s_add_u32 s0, s0, 0x2400
	s_addc_u32 s1, s1, 0
	v_writelane_b32 v252, s9, 11
	v_writelane_b32 v252, s0, 12
	s_nop 1
	v_writelane_b32 v252, s1, 13
	s_add_u32 s0, s26, 0x7400
	s_addc_u32 s1, s27, 0
	v_writelane_b32 v252, s0, 14
	s_nop 1
	v_writelane_b32 v252, s1, 15
	v_readlane_b32 s0, v249, 28
	s_cmpk_lt_u32 s0, 0xa4
	s_cselect_b64 s[0:1], -1, 0
	v_writelane_b32 v252, s0, 16
	s_nop 1
	v_writelane_b32 v252, s1, 17
	v_readlane_b32 s0, v249, 28
	s_add_i32 s60, s0, 0xffffff60
	s_mul_i32 s0, s60, 0xc000
	s_add_u32 s0, s26, s0
	s_mul_hi_u32 s1, s60, 0xc000
	s_addc_u32 s1, s27, s1
	s_add_u32 s0, s0, 0x106000
	s_addc_u32 s1, s1, 0
	v_writelane_b32 v252, s0, 18
	s_lshl_b64 s[8:9], s[60:61], 6
	s_nop 0
	v_writelane_b32 v252, s1, 19
	s_add_u32 s0, s7, s8
	s_addc_u32 s1, s43, s9
	v_writelane_b32 v252, s0, 20
	s_add_i32 s30, s58, 0xffffff80
	s_nop 0
	v_writelane_b32 v252, s1, 21
	v_readlane_b32 s0, v249, 28
	s_cmpk_lt_u32 s0, 0x1a70
	s_cselect_b64 s[0:1], -1, 0
	v_writelane_b32 v252, s0, 22
	s_cmpk_gt_u32 s31, 0x1df
	s_cselect_b64 s[8:9], -1, 0
	v_writelane_b32 v252, s1, 23
	s_waitcnt vmcnt(15)
	v_sub_co_u32_e64 v2, s[0:1], s31, v1
	s_nop 1
	v_writelane_b32 v252, s0, 24
	s_nop 1
	v_writelane_b32 v252, s1, 25
	v_readfirstlane_b32 s0, v2
	v_mov_b32_e32 v2, 0x2e0
	v_writelane_b32 v252, s8, 26
	v_sub_co_u32_e64 v3, s[34:35], s31, v2
	s_nop 0
	v_writelane_b32 v252, s9, 27
	s_lshr_b32 s1, s0, 7
	s_xor_b64 s[8:9], s[34:35], -1
	s_add_i32 s60, s21, s1
	v_writelane_b32 v252, s8, 28
	s_lshl_b32 s0, s0, 3
	s_and_b32 s0, s0, 0x380
	v_writelane_b32 v252, s9, 29
	s_lshl_b64 s[8:9], s[60:61], 23
	s_add_u32 s1, s84, s8
	s_addc_u32 s5, s85, s9
	s_lshl_b32 s8, s0, 13
	s_add_u32 s1, s1, s8
	s_addc_u32 s8, s5, 0
	s_lshl_b32 s5, s31, 7
	s_and_b32 s10, s5, 0x700
	s_lshl_b32 s11, s10, 2
	s_add_u32 s1, s1, s11
	v_writelane_b32 v252, s1, 30
	s_addc_u32 s1, s8, 0
	s_add_u32 s2, s26, 0x14400000
	s_addc_u32 s44, s27, 0
	s_lshl_b64 s[8:9], s[60:61], 22
	v_writelane_b32 v252, s1, 31
	s_add_u32 s1, s2, s8
	s_addc_u32 s8, s44, s9
	s_lshl_b32 s9, s10, 11
	s_add_u32 s1, s1, s9
	s_addc_u32 s8, s8, 0
	s_lshl_b32 s0, s0, 1
	s_add_u32 s0, s1, s0
	v_writelane_b32 v252, s0, 33
	s_addc_u32 s0, s8, 0
	v_writelane_b32 v252, s0, 35
	v_readfirstlane_b32 s0, v3
	s_and_b32 s1, s31, 6
	s_cmpk_lt_u32 s0, 0x800
	s_cselect_b32 s8, s81, s83
	s_cselect_b32 s9, s80, s82
	s_lshl_b32 s28, s0, 4
	s_and_b32 s29, s28, 0x7800
	s_or_b32 s29, s20, s29
	s_and_b32 s28, s28, 0x780
	s_or_b32 s34, s29, s28
	s_lshl_b32 s34, s34, 12
	s_add_u32 s9, s9, s34
	s_addc_u32 s8, s8, 0
	s_lshl_b32 s34, s1, 9
	s_add_u32 s5, s9, s34
	v_writelane_b32 v252, s5, 37
	s_addc_u32 s5, s8, 0
	s_add_u32 s96, s26, 0x4400000
	s_addc_u32 s97, s27, 0
	s_lshr_b32 s0, s0, 4
	s_lshl_b32 s1, s1, 8
	s_and_b32 s0, s0, 0xfffff80
	s_add_i32 s0, s0, s1
	s_add_i32 s60, s29, s0
	s_lshl_b64 s[8:9], s[60:61], 12
	s_add_u32 s0, s96, s8
	s_addc_u32 s1, s97, s9
	s_lshl_b32 s8, s28, 1
	v_writelane_b32 v252, s5, 38
	s_add_u32 s0, s0, s8
	v_writelane_b32 v252, s0, 39
	s_addc_u32 s0, s1, 0
	v_writelane_b32 v252, s0, 40
	s_lshl_b32 s0, s31, 3
	s_and_b32 s0, s0, 0x1f80
	s_add_i32 s60, s0, 0xfffff100
	s_add_i32 s8, s18, s60
	s_mov_b32 s9, s61
	s_lshl_b64 s[8:9], s[8:9], 13
	s_add_u32 s0, s74, s8
	s_addc_u32 s1, s75, s9
	s_add_u32 s0, s0, s11
	s_addc_u32 s1, s1, 0
	v_writelane_b32 v252, s0, 41
	s_nop 1
	v_writelane_b32 v252, s1, 42
	s_lshl_b32 s0, s18, 2
	s_add_u32 s0, s72, s0
	s_addc_u32 s1, s73, 0
	s_lshl_b64 s[8:9], s[60:61], 2
	s_add_u32 s0, s0, s8
	s_addc_u32 s1, s1, s9
	v_writelane_b32 v252, s0, 43
	s_add_u32 s92, s26, 0x3400000
	s_addc_u32 s93, s27, 0
	v_writelane_b32 v252, s1, 44
	s_or_b32 s0, s18, s10
	s_lshl_b32 s0, s0, 12
	s_add_u32 s0, s92, s0
	s_addc_u32 s1, s93, 0
	s_lshl_b64 s[8:9], s[60:61], 1
	s_add_u32 s0, s0, s8
	s_addc_u32 s1, s1, s9
	v_writelane_b32 v252, s0, 45
	s_nop 1
	v_writelane_b32 v252, s1, 46
	s_mul_i32 s0, s31, 0x8889
	s_lshr_b32 s1, s0, 20
	s_lshr_b32 s0, s0, 13
	s_and_b32 s34, s0, 0xff80
	s_mul_i32 s1, s1, 30
	s_add_i32 s0, s18, s34
	s_sub_i32 s1, s31, s1
	s_mulk_i32 s0, 0x3c00
	s_add_u32 s0, s52, s0
	s_addc_u32 s8, s53, 0
	s_lshl_b32 s9, s1, 7
	s_and_b32 s64, s9, 0xff80
	s_lshl_b32 s9, s64, 2
	s_add_u32 s10, s0, s9
	s_addc_u32 s11, s8, 0
	v_writelane_b32 v252, s10, 47
	s_and_b32 s0, s1, 0xffff
	s_nop 0
	v_writelane_b32 v252, s11, 48
	v_writelane_b32 v252, s0, 49
	s_add_i32 s0, s64, 0xfffffe00
	s_add_u32 s5, s0, s13
	s_addc_u32 s22, 0, 0
	s_add_u32 s23, s38, s23
	s_addc_u32 s59, s39, 0
	v_sub_co_u32_e64 v3, s[0:1], s19, v1
	s_cmpk_gt_u32 s19, 0x1df
	s_nop 0
	v_writelane_b32 v252, s0, 50
	s_cselect_b64 s[8:9], -1, 0
	s_nop 0
	v_writelane_b32 v252, s1, 51
	v_readfirstlane_b32 s0, v3
	v_writelane_b32 v252, s8, 52
	v_sub_co_u32_e64 v3, s[36:37], s19, v2
	s_nop 0
	v_writelane_b32 v252, s9, 53
	s_lshr_b32 s1, s0, 7
	s_xor_b64 s[8:9], s[36:37], -1
	s_add_i32 s60, s21, s1
	v_writelane_b32 v252, s8, 54
	s_lshl_b32 s0, s0, 3
	s_and_b32 s0, s0, 0x380
	v_writelane_b32 v252, s9, 55
	s_lshl_b64 s[8:9], s[60:61], 23
	s_add_u32 s1, s84, s8
	s_addc_u32 s8, s85, s9
	s_lshl_b32 s9, s0, 13
	s_add_u32 s1, s1, s9
	s_addc_u32 s8, s8, 0
; __device__ __forceinline__ bool tdecode(const Params& p, int it, TDesc& d) {
;     if (it >= 2 * 6880) return false;
;     const int l = it / 6880; int r = it % 6880;
;     d.ksc = nullptr;
;     if (r < 480) { const int kt = r / 30, nt = r % 30;
;         d.src = p.in[6] + ((size_t)l * 2048 + kt * 128) * DIN + nt * 128; d.lds_ = DIN;
;         d.dst = (nt < 4 ? (bf16_t*)(p.ws + WS_WPQ) + ((size_t)l * 512 + nt * 128) * 2048 : (bf16_t*)(p.ws + WS_WIN) + ((size_t)l * NPROJ + (nt - 4) * 128) * 2048) + kt * 128; d.ldd = 2048; return true; }
;     r -= 480;
;     if (r < 256) { const int kt = r / 16, nt = r % 16;
;         d.src = p.in[13] + ((size_t)l * 2048 + kt * 128) * 2048 + nt * 128; d.lds_ = 2048; d.ksc = p.in[12] + (size_t)l * 2048 + kt * 128;
;         d.dst = (bf16_t*)(p.ws + WS_WOUT) + ((size_t)l * 2048 + nt * 128) * 2048 + kt * 128; d.ldd = 2048; return true; }
;     r -= 256;
;     if (r < 4096) { const int isup = r / 2048, r2 = r % 2048, e = r2 / 128, kt = (r2 % 128) / 8, nt = r2 % 8;
;         d.src = p.in[isup ? 17 : 16] + (((size_t)l * 16 + e) * 2048 + kt * 128) * 1024 + nt * 128; d.lds_ = 1024;
;         d.dst = (bf16_t*)(p.ws + WS_WGU) + (((size_t)l * 16 + e) * 2048 + nt * 256 + isup * 128) * 2048 + kt * 128; d.ldd = 2048; return true; }
;     r -= 4096;
;     { const int e = r / 128, kt = (r % 128) / 16, nt = r % 16;
;         d.src = p.in[18] + (((size_t)l * 16 + e) * 1024 + kt * 128) * 2048 + nt * 128; d.lds_ = 2048;
;         d.dst = (bf16_t*)(p.ws + WS_WD) + (((size_t)l * 16 + e) * 2048 + nt * 128) * 1024 + kt * 128; d.ldd = 1024; return true; }
; }
	s_lshl_b32 s9, s19, 7
	s_and_b32 s10, s9, 0x780
	s_lshl_b32 s11, s10, 2
	s_add_u32 s79, s1, s11
	s_addc_u32 s35, s8, 0
	s_lshl_b64 s[8:9], s[60:61], 22
	s_add_u32 s1, s2, s8
	s_addc_u32 s8, s44, s9
	s_lshl_b32 s9, s10, 11
	s_add_u32 s1, s1, s9
	s_addc_u32 s8, s8, 0
	s_lshl_b32 s0, s0, 1
	s_add_u32 s0, s1, s0
	v_writelane_b32 v252, s0, 56
	s_addc_u32 s0, s8, 0
	v_writelane_b32 v252, s0, 57
	v_readfirstlane_b32 s0, v3
	s_and_b32 s1, s19, 7
	s_cmpk_lt_u32 s0, 0x800
	s_cselect_b32 s8, s81, s83
	s_cselect_b32 s9, s80, s82
	s_lshl_b32 s21, s0, 4
	s_and_b32 s28, s21, 0x7800
	s_or_b32 s20, s20, s28
	s_and_b32 s21, s21, 0x780
	s_or_b32 s28, s20, s21
	s_lshl_b32 s28, s28, 12
	s_add_u32 s9, s9, s28
	s_addc_u32 s8, s8, 0
	s_lshl_b32 s28, s1, 9
	s_add_u32 s6, s9, s28
	s_addc_u32 s70, s8, 0
	s_lshr_b32 s0, s0, 4
	s_lshl_b32 s1, s1, 8
	s_and_b32 s0, s0, 0xfffff80
	s_add_i32 s0, s0, s1
	s_add_i32 s60, s20, s0
	s_lshl_b64 s[8:9], s[60:61], 12
	s_add_u32 s0, s96, s8
	s_addc_u32 s1, s97, s9
	s_lshl_b32 s8, s21, 1
	s_add_u32 s71, s0, s8
	s_addc_u32 s76, s1, 0
	s_lshl_b32 s0, s19, 3
	s_and_b32 s0, s0, 0x1f80
	s_add_i32 s60, s0, 0xfffff100
	s_add_i32 s8, s18, s60
	s_mov_b32 s9, s61
	s_lshl_b64 s[8:9], s[8:9], 13
	s_add_u32 s0, s74, s8
	s_addc_u32 s1, s75, s9
	s_add_u32 s0, s0, s11
	v_writelane_b32 v252, s6, 58
	s_addc_u32 s1, s1, 0
	v_writelane_b32 v252, s0, 60
	s_nop 1
	v_writelane_b32 v252, s1, 61
	s_or_b32 s0, s18, s10
	s_lshl_b32 s0, s0, 12
	s_add_u32 s0, s92, s0
	s_addc_u32 s1, s93, 0
	s_lshl_b64 s[8:9], s[60:61], 1
	s_add_u32 s0, s0, s8
	s_addc_u32 s1, s1, s9
	v_writelane_b32 v252, s0, 62
	s_nop 1
	v_writelane_b32 v252, s1, 63
	s_mul_i32 s0, s19, 0x8889
	s_lshr_b32 s1, s0, 20
	s_lshr_b32 s0, s0, 13
	s_and_b32 s77, s0, 0xff80
	s_mul_i32 s1, s1, 30
	s_add_i32 s0, s18, s77
	s_sub_i32 s1, s19, s1
	s_mulk_i32 s0, 0x3c00
	s_add_u32 s0, s52, s0
	s_addc_u32 s8, s53, 0
	s_lshl_b32 s9, s1, 7
	s_and_b32 s65, s9, 0xff80
	s_lshl_b32 s9, s65, 2
	s_add_u32 s10, s0, s9
	s_addc_u32 s11, s8, 0
	s_and_b32 s69, s1, 0xffff
	s_add_i32 s0, s65, 0xfffffe00
	s_add_u32 s78, s0, s13
	s_addc_u32 s68, 0, 0
	s_add_i32 s0, s30, s12
	v_writelane_b32 v253, s10, 0
	s_cmpk_lt_u32 s0, 0x1ae0
	s_cselect_b64 s[8:9], -1, 0
	v_writelane_b32 v253, s11, 1
	s_lshl_b32 s1, s0, 1
	v_writelane_b32 v253, s8, 2
	s_cmpk_gt_u32 s0, 0xd6f
	s_nop 0
	v_writelane_b32 v253, s9, 3
	s_cselect_b64 s[8:9], -1, 0
	s_add_i32 s10, s1, 0xffffe520
	s_or_b32 s11, s1, 1
	s_add_i32 s12, s1, 0xffffe521
	s_cmpk_lt_u32 s0, 0xd70
	s_cselect_b32 s0, s1, s10
	s_cselect_b32 s18, s11, s12
	s_cmpk_gt_i32 s0, 0x1df
	s_cselect_b64 s[10:11], -1, 0
	v_sub_co_u32_e64 v3, s[36:37], s0, v2
	v_writelane_b32 v253, s10, 4
	v_sub_co_u32_e64 v4, s[66:67], s0, v1
	s_nop 0
	v_writelane_b32 v253, s11, 5
	s_xor_b64 s[10:11], s[36:37], -1
	v_readfirstlane_b32 s1, v4
	v_writelane_b32 v253, s10, 6
	s_lshr_b32 s12, s1, 7
	s_nop 0
	v_writelane_b32 v253, s11, 7
	s_and_b64 s[10:11], s[8:9], exec
	s_cselect_b32 s19, 16, 0
	s_add_i32 s60, s19, s12
	s_lshl_b32 s1, s1, 3
	s_and_b32 s1, s1, 0x380
	s_lshl_b64 s[10:11], s[60:61], 23
	s_add_u32 s10, s84, s10
	s_addc_u32 s11, s85, s11
	s_lshl_b32 s12, s1, 13
	s_add_u32 s10, s10, s12
	s_addc_u32 s11, s11, 0
	s_lshl_b32 s12, s0, 7
	s_and_b32 s12, s12, 0x700
	s_lshl_b32 s13, s12, 2
	s_add_u32 s86, s10, s13
	s_addc_u32 s87, s11, 0
	s_lshl_b64 s[10:11], s[60:61], 22
	s_add_u32 s10, s2, s10
	s_addc_u32 s11, s44, s11
	s_lshl_b32 s20, s12, 11
	s_add_u32 s10, s10, s20
	s_addc_u32 s11, s11, 0
	s_lshl_b32 s1, s1, 1
	s_add_u32 s6, s10, s1
	s_addc_u32 s36, s11, 0
	s_and_b32 s1, s0, 6
	v_readfirstlane_b32 s20, v3
	s_cmpk_lt_u32 s20, 0x800
	s_cselect_b32 s21, s81, s83
	s_cselect_b32 s28, s80, s82
	s_lshl_b32 s29, s20, 4
	s_and_b32 s31, s29, 0x7800
	s_and_b64 s[10:11], s[8:9], exec
	s_cselect_b32 s33, 0x8000, 0
	s_or_b32 s10, s33, s31
	s_and_b32 s29, s29, 0x780
	s_or_b32 s11, s10, s29
	s_lshl_b32 s11, s11, 12
	s_add_u32 s11, s28, s11
	s_addc_u32 s21, s21, 0
	s_lshl_b32 s28, s1, 9
	s_add_u32 s37, s11, s28
	s_addc_u32 s57, s21, 0
	s_lshr_b32 s11, s20, 4
	s_lshl_b32 s1, s1, 8
	s_and_b32 s11, s11, 0xfffff80
	s_add_i32 s11, s11, s1
	s_add_i32 s60, s10, s11
	s_lshl_b64 s[10:11], s[60:61], 12
	s_add_u32 s1, s96, s10
	s_addc_u32 s10, s97, s11
	s_lshl_b32 s11, s29, 1
	s_add_u32 s88, s1, s11
	s_addc_u32 s89, s10, 0
	s_and_b64 s[10:11], s[8:9], exec
	s_cselect_b32 s1, 0x800, 0
	s_lshl_b32 s10, s0, 3
	s_and_b32 s10, s10, 0x1f80
	s_add_i32 s60, s10, 0xfffff100
	s_add_i32 s10, s1, s60
	s_mov_b32 s11, s61
	s_lshl_b64 s[10:11], s[10:11], 13
	s_add_u32 s10, s74, s10
	s_addc_u32 s11, s75, s11
	s_add_u32 s10, s10, s13
	s_addc_u32 s11, s11, 0
	v_writelane_b32 v253, s10, 8
	s_nop 1
	v_writelane_b32 v253, s11, 9
	s_lshl_b32 s10, s1, 2
	s_add_u32 s13, s72, s10
	s_addc_u32 s20, s73, 0
	s_lshl_b64 s[10:11], s[60:61], 2
	s_add_u32 s10, s13, s10
	s_addc_u32 s11, s20, s11
	v_writelane_b32 v253, s10, 10
	s_nop 1
	v_writelane_b32 v253, s11, 11
	s_or_b32 s10, s1, s12
	s_lshl_b32 s10, s10, 12
	s_add_u32 s12, s92, s10
	s_addc_u32 s13, s93, 0
	s_lshl_b64 s[10:11], s[60:61], 1
	s_add_u32 s10, s12, s10
	s_addc_u32 s11, s13, s11
	v_writelane_b32 v253, s10, 12
	s_nop 1
	v_writelane_b32 v253, s11, 13
	s_sext_i32_i16 s10, s0
	s_mulk_i32 s10, 0x8889
	s_lshr_b32 s10, s10, 16
	s_add_i32 s10, s10, s0
	s_sext_i32_i16 s11, s10
	s_ashr_i32 s11, s11, 4
	s_bfe_u32 s10, s10, 0x1000f
	s_add_i32 s10, s11, s10
	s_mul_i32 s11, s10, 30
	s_sext_i32_i16 s10, s10
	s_sub_i32 s0, s0, s11
	s_lshl_b32 s10, s10, 7
	s_sext_i32_i16 s90, s0
	s_add_i32 s0, s1, s10
	s_ashr_i32 s11, s10, 31
	s_mul_hi_i32 s12, s0, 0x3c00
	s_mulk_i32 s0, 0x3c00
	s_add_u32 s0, s52, s0
	s_addc_u32 s28, s53, s12
; #define LAS __attribute__((address_space(3)))
; __device__ __forceinline__ bool tdecode(const Params& p, int it, TDesc& d) {
;     if (it >= 2 * 6880) return false;
;     const int l = it / 6880; int r = it % 6880;
;     d.ksc = nullptr;
;     if (r < 480) { const int kt = r / 30, nt = r % 30;
;         d.src = p.in[6] + ((size_t)l * 2048 + kt * 128) * DIN + nt * 128; d.lds_ = DIN;
;         d.dst = (nt < 4 ? (bf16_t*)(p.ws + WS_WPQ) + ((size_t)l * 512 + nt * 128) * 2048 : (bf16_t*)(p.ws + WS_WIN) + ((size_t)l * NPROJ + (nt - 4) * 128) * 2048) + kt * 128; d.ldd = 2048; return true; }
;     r -= 480;
;     if (r < 256) { const int kt = r / 16, nt = r % 16;
;         d.src = p.in[13] + ((size_t)l * 2048 + kt * 128) * 2048 + nt * 128; d.lds_ = 2048; d.ksc = p.in[12] + (size_t)l * 2048 + kt * 128;
;         d.dst = (bf16_t*)(p.ws + WS_WOUT) + ((size_t)l * 2048 + nt * 128) * 2048 + kt * 128; d.ldd = 2048; return true; }
;     r -= 256;
;     if (r < 4096) { const int isup = r / 2048, r2 = r % 2048, e = r2 / 128, kt = (r2 % 128) / 8, nt = r2 % 8;
;         d.src = p.in[isup ? 17 : 16] + (((size_t)l * 16 + e) * 2048 + kt * 128) * 1024 + nt * 128; d.lds_ = 1024;
;         d.dst = (bf16_t*)(p.ws + WS_WGU) + (((size_t)l * 16 + e) * 2048 + nt * 256 + isup * 128) * 2048 + kt * 128; d.ldd = 2048; return true; }
;     r -= 4096;
;     { const int e = r / 128, kt = (r % 128) / 16, nt = r % 16;
;         d.src = p.in[18] + (((size_t)l * 16 + e) * 1024 + kt * 128) * 2048 + nt * 128; d.lds_ = 2048;
;         d.dst = (bf16_t*)(p.ws + WS_WD) + (((size_t)l * 16 + e) * 2048 + nt * 128) * 1024 + kt * 128; d.ldd = 1024; return true; }
; }
; __device__ __forceinline__ void ph_mixers(const Params& p, const int l, LAS unsigned char* lds, const int vbx, const int vG) {
;     constexpr int VTS = 260, VTSS = 292, KSTR = 72, ARENA = 78848, KOFF = 37376;
;     const int hw = (opaque_tid() >> 8) & 1;
;     const bf16_t* PROJ = (const bf16_t*)(p.ws + WS_PROJ);
;     int ufirst, ucount, ustep;
;     if (vG == 256) { if (vbx < 128) { ufirst = vbx * 2; ucount = 2; } else { ufirst = 256 + (vbx - 128) * 4; ucount = 4; } ustep = 1; }
;     else { ufirst = vbx; ustep = vG; ucount = (768 - vbx + vG - 1) / vG; }
;     const int nsw = (256 - vbx + vG - 1) / vG;
;     const int ngm = vbx < 128 ? (128 - vbx + vG - 1) / vG : 0;
;     const int nitems = ngm + nsw + ucount;
	s_lshl_b32 s12, s90, 7
	s_ashr_i32 s13, s12, 31
	s_lshl_b64 s[20:21], s[12:13], 2
	s_add_u32 s20, s0, s20
	s_addc_u32 s21, s28, s21
	v_writelane_b32 v253, s20, 14
	s_nop 1
	v_writelane_b32 v253, s21, 15
	s_and_b64 s[20:21], s[8:9], exec
	s_cselect_b32 s0, 0xd00, 0
	s_add_i32 s91, s12, s0
	s_addk_i32 s91, 0xfe00
	s_and_b64 s[8:9], s[8:9], exec
	s_cselect_b32 s8, 0x200000, 0
	v_writelane_b32 v253, s38, 16
	s_add_u32 s8, s38, s8
	v_writelane_b32 v253, s39, 17
	s_addc_u32 s9, s39, 0
	v_sub_co_u32_e64 v1, s[38:39], s18, v1
	s_cmpk_gt_i32 s18, 0x1df
	v_readfirstlane_b32 s20, v1
	s_cselect_b64 s[28:29], -1, 0
	s_lshr_b32 s21, s20, 7
	v_writelane_b32 v253, s28, 18
	s_add_i32 s60, s19, s21
	v_sub_co_u32_e64 v1, s[40:41], s18, v2
	s_lshl_b32 s19, s20, 3
	v_writelane_b32 v253, s29, 19
	s_xor_b64 s[28:29], s[40:41], -1
	s_and_b32 s19, s19, 0x380
	s_lshl_b64 s[20:21], s[60:61], 23
	v_writelane_b32 v253, s28, 20
	s_add_u32 s20, s84, s20
	s_addc_u32 s21, s85, s21
	v_writelane_b32 v253, s29, 21
	s_lshl_b32 s28, s19, 13
	s_add_u32 s20, s20, s28
	s_addc_u32 s21, s21, 0
	s_lshl_b32 s28, s18, 7
	s_and_b32 s28, s28, 0x780
	s_lshl_b32 s29, s28, 2
	s_add_u32 s40, s20, s29
	s_addc_u32 s41, s21, 0
	s_lshl_b64 s[20:21], s[60:61], 22
	s_add_u32 s20, s2, s20
	s_addc_u32 s21, s44, s21
	s_lshl_b32 s31, s28, 11
	s_add_u32 s20, s20, s31
	s_addc_u32 s21, s21, 0
	s_lshl_b32 s19, s19, 1
	s_add_u32 s48, s20, s19
	s_addc_u32 s49, s21, 0
	s_and_b32 s19, s18, 7
	v_readfirstlane_b32 s20, v1
	s_cmpk_lt_u32 s20, 0x800
	s_cselect_b32 s21, s81, s83
	s_cselect_b32 s31, s80, s82
	s_lshl_b32 s47, s20, 4
	s_and_b32 s56, s47, 0x7800
	s_or_b32 s46, s33, s56
	s_and_b32 s47, s47, 0x780
	s_or_b32 s56, s46, s47
	s_lshl_b32 s56, s56, 12
	s_add_u32 s31, s31, s56
	s_addc_u32 s21, s21, 0
	s_lshl_b32 s56, s19, 9
	s_add_u32 s94, s31, s56
	s_addc_u32 s95, s21, 0
	s_lshr_b32 s20, s20, 4
	s_lshl_b32 s19, s19, 8
	s_and_b32 s20, s20, 0xfffff80
	s_add_i32 s20, s20, s19
	s_add_i32 s60, s46, s20
	s_lshl_b64 s[20:21], s[60:61], 12
	v_writelane_b32 v253, s2, 22
	s_add_u32 s19, s96, s20
	v_writelane_b32 v253, s44, 23
	s_addc_u32 s20, s97, s21
	s_lshl_b32 s21, s47, 1
	v_writelane_b32 v253, s96, 24
	s_add_u32 s96, s19, s21
	v_writelane_b32 v253, s97, 25
	s_addc_u32 s97, s20, 0
	s_lshl_b32 s19, s18, 3
	s_and_b32 s19, s19, 0x1f80
	s_add_i32 s60, s19, 0xfffff100
	s_add_i32 s20, s1, s60
	s_mov_b32 s21, s61
	s_lshl_b64 s[20:21], s[20:21], 13
	s_add_u32 s19, s74, s20
	s_addc_u32 s20, s75, s21
	s_add_u32 s44, s19, s29
	s_addc_u32 s45, s20, 0
	s_or_b32 s19, s1, s28
	s_lshl_b32 s19, s19, 12
	s_add_u32 s19, s92, s19
	v_writelane_b32 v253, s44, 26
	s_addc_u32 s28, s93, 0
	s_lshl_b64 s[20:21], s[60:61], 1
	v_writelane_b32 v253, s45, 27
	s_add_u32 s20, s19, s20
	s_sext_i32_i16 s19, s18
	v_writelane_b32 v253, s92, 28
	s_mulk_i32 s19, 0x8889
	v_writelane_b32 v253, s93, 29
	s_addc_u32 s21, s28, s21
	s_lshr_b32 s19, s19, 16
	v_writelane_b32 v253, s20, 30
	s_add_i32 s19, s19, s18
	v_readlane_b32 s33, v250, 51
	v_writelane_b32 v253, s21, 31
	s_sext_i32_i16 s20, s19
	s_ashr_i32 s20, s20, 4
	s_bfe_u32 s19, s19, 0x1000f
	s_add_i32 s19, s20, s19
	s_mul_i32 s20, s19, 30
	s_sub_i32 s18, s18, s20
	s_sext_i32_i16 s19, s19
	s_sext_i32_i16 s56, s18
	s_lshl_b32 s18, s19, 7
	s_add_i32 s1, s1, s18
	s_ashr_i32 s19, s18, 31
	s_mul_hi_i32 s20, s1, 0x3c00
	s_mulk_i32 s1, 0x3c00
	s_add_u32 s1, s52, s1
	s_addc_u32 s28, s53, s20
	s_lshl_b32 s20, s56, 7
	s_ashr_i32 s21, s20, 31
	s_lshl_b64 s[46:47], s[20:21], 2
	s_add_u32 s44, s1, s46
	s_addc_u32 s45, s28, s47
	v_writelane_b32 v253, s44, 32
	s_add_i32 s60, s20, s0
	s_addk_i32 s60, 0xfe00
	v_writelane_b32 v253, s45, 33
	s_lshl_b32 s0, s30, 1
	v_writelane_b32 v253, s0, 34
	s_add_u32 s0, s26, 0x200000
	s_addc_u32 s1, s27, 0
	v_writelane_b32 v253, s0, 35
	v_readlane_b32 s2, v249, 28
	s_mov_b64 s[46:47], s[62:63]
	v_writelane_b32 v253, s1, 36
	s_add_u32 s0, s26, 0x204000
	s_addc_u32 s1, s27, 0
	v_writelane_b32 v253, s0, 37
	v_mbcnt_lo_u32_b32 v1, -1, 0
	v_mbcnt_hi_u32_b32 v212, -1, v1
	v_writelane_b32 v253, s1, 38
	s_add_u32 s0, s26, 0x208000
	s_addc_u32 s1, s27, 0
	v_writelane_b32 v253, s0, 39
	v_and_b32_e32 v226, 64, v212
	v_add_u32_e32 v213, 64, v226
	v_writelane_b32 v253, s1, 40
	s_add_u32 s0, s26, 0x2a800000
	s_addc_u32 s1, s27, 0
	v_writelane_b32 v253, s0, 41
	v_xor_b32_e32 v220, 1, v212
	v_xor_b32_e32 v216, 16, v212
	v_writelane_b32 v253, s1, 42
	s_add_u32 s0, s26, 0x20a000
	s_addc_u32 s1, s27, 0
	v_writelane_b32 v253, s0, 43
	s_nop 1
	v_writelane_b32 v253, s1, 44
	v_readlane_b32 s0, v249, 28
	s_cmpk_lt_i32 s0, 0x100
	s_cselect_b64 s[0:1], -1, 0
	v_writelane_b32 v253, s0, 45
	s_nop 1
	v_writelane_b32 v253, s1, 46
	v_readlane_b32 s0, v249, 28
	s_ashr_i32 s30, s0, 6
	s_ashr_i32 s31, s30, 31
	s_lshl_b64 s[30:31], s[30:31], 21
	s_add_u32 s0, s33, s30
	s_addc_u32 s1, s3, s31
	s_lshl_b32 s28, s2, 15
	s_and_b32 s28, s28, 0x1f8000
	s_add_u32 s0, s0, s28
	v_writelane_b32 v253, s3, 47
	s_addc_u32 s1, s1, 0
	v_writelane_b32 v253, s0, 48
	s_nop 1
	v_writelane_b32 v253, s1, 49
	v_readlane_b32 s0, v249, 28
	s_lshl_b32 s0, s0, 2
	v_readlane_b32 s1, v249, 28
	s_addk_i32 s0, 0xff00
	s_lshl_b32 s44, s1, 1
	s_and_b64 s[30:31], vcc, exec
	s_cmpk_lt_u32 s1, 0x80
	s_cselect_b32 s0, s44, s0
	v_writelane_b32 v253, s0, 50
	s_cselect_b32 s0, 2, 4
	v_writelane_b32 v253, s0, 51
	v_readlane_b32 s0, v249, 28
	s_sub_i32 s0, 0x100, s0
	s_nop 0
	v_writelane_b32 v253, s0, 52
	s_add_u32 s0, s26, 0x3b300000
	v_writelane_b32 v253, s0, 53
	s_addc_u32 s0, s27, 0
	v_writelane_b32 v253, s0, 54
	s_add_u32 s0, s26, 0x2d800000
	s_addc_u32 s1, s27, 0
	v_writelane_b32 v253, s0, 55
	s_nop 1
	v_writelane_b32 v253, s1, 56
	s_add_u32 s0, s26, 0x2f000000
; __global__ void __launch_bounds__(512, 2) mk_fwd(Params p) {
;     ...
;             SchedDense S{(const char*)(p.ws + WS_YN), (const char*)(p.ws + WS_WOUT) + (size_t)l * 2048 * 2048 * 2, 32, 8, 2048, G, bx};
;             const float* modl = (const float*)(p.ws + WS_MOD) + (size_t)l * 4 * 12288;
;             if (G == 256) {
;                 float* xch = (float*)(p.ws + WS_XE + (size_t)l * 8 * MiB);
;                 EpiWoutN E{l == 0 ? p.in[0] : nullptr, (const bf16_t*)(p.ws + WS_X), (bf16_t*)(p.ws + WS_X2), modl + 2 * 2048, p.in[14] + (size_t)l * DM, modl + 3 * 2048,
;                            (const bf16_t*)(p.ws + WS_WRT) + (size_t)l * 16 * 2048, (bf16_t*)(p.ws + WS_H), (float*)(p.ws + WS_AFF), (const float*)(p.ws + WS_XE + 16 * MiB) + (size_t)l * 64,
;                            xch, xch + 262144, (unsigned*)(p.ws + WS_CTL) + CTL_PANEL + (size_t)l * 32 * 64, (unsigned*)(p.ws + WS_CTL), (unsigned*)(p.ws + WS_CTL) + CTL_PANEL + 4096 + 1024 + (size_t)l * 1024};
;                 pg8::gemm_phase<EpiWoutN, SchedDense>(lds, 2048, 2048, 2048, S, E);
;             } else {
;                 EpiWout E{l == 0 ? p.in[0] : nullptr, (const bf16_t*)(p.ws + WS_X), (bf16_t*)(p.ws + WS_X2), modl + 2 * 2048};
;                 pg8::gemm_phase<EpiWout, SchedDense>(lds, 2048, 2048, 2048, S, E);
;             }
;         }
;         if (G != 256) {
;             SEAM(pb + 4);
;             if (EN(11) && IN(pb + 5)) REP(11) { ph_norm2_router_mfma(p, l, lds); }
;             SEAM(pb + 5);
;             if (EN(12) && IN(pb + 6)) REP(12) { ph_topk(p, lds); }
;         } else if (EN(12) && IN(pb + 6)) {
;             __syncthreads();
;             ph_topk(p, lds, (const unsigned*)(p.ws + WS_CTL) + CTL_PANEL + 4096 + 1024 + (size_t)l * 1024);
;             if (split_ok && l == 0 && bx >= 64 && bx < 68) ph_rbias(p, 1, bx - 64);
;         }
;         SEAM(pb + 6);
;         if (EN(14) && IN(pb + 8)) REP(14) {
;             SchedMoeG S{H, (const char*)(p.ws + WS_WGU) + (size_t)l * 16 * 2048 * 2048 * 2, 2048, G, bx};
;             EpiGU E{(bf16_t*)(p.ws + WS_ACT)};
;             pg8::gemm_phase<EpiGU, SchedMoeG, true>(lds, 2048, 2048, 2048, S, E, (const int*)(p.ws + WS_IDX));
;         }
;         SEAM(pb + 8);
;         if (EN(15) && IN(pb + 9)) REP(15) {
;             SchedMoe S{(const char*)(p.ws + WS_ACT), (const char*)(p.ws + WS_WD) + (size_t)l * 16 * 2048 * 1024 * 2, 1024, G, bx};
	s_addc_u32 s1, s27, 0
	v_writelane_b32 v253, s0, 57
	s_nop 1
	v_writelane_b32 v253, s1, 58
	s_add_u32 s0, s26, 0x2d000000
	s_addc_u32 s1, s27, 0
	v_writelane_b32 v253, s0, 59
	s_nop 1
	v_writelane_b32 v253, s1, 60
	s_add_u32 s0, s26, 0x2c800000
	s_addc_u32 s1, s27, 0
	v_writelane_b32 v253, s0, 61
	s_nop 1
	v_writelane_b32 v253, s1, 62
	s_add_u32 s0, s26, 0x3b3e0000
	s_addc_u32 s1, s27, 0
	v_writelane_b32 v253, s0, 63
	s_nop 1
	v_writelane_b32 v254, s1, 0
	s_add_u32 s0, s26, 0x3b3a0000
	s_addc_u32 s1, s27, 0
	s_add_u32 s72, s26, 0x2f100000
	v_writelane_b32 v254, s0, 1
	s_addc_u32 s73, s27, 0
	s_nop 0
	v_writelane_b32 v254, s1, 2
	s_add_u32 s0, s26, 0x31300000
	v_writelane_b32 v254, s0, 3
	s_addc_u32 s0, s27, 0
	v_writelane_b32 v254, s0, 4
	s_add_u32 s0, s26, 0x31100000
	s_addc_u32 s1, s27, 0
	v_writelane_b32 v254, s0, 5
	s_nop 1
	v_writelane_b32 v254, s1, 6
	s_add_u32 s0, s26, 0x8000
	v_writelane_b32 v254, s0, 7
	s_addc_u32 s0, s27, 0
	v_writelane_b32 v254, s0, 8
	s_add_u32 s0, s26, 0xd000
	v_writelane_b32 v254, s0, 9
	s_addc_u32 s0, s27, 0
	s_add_u32 s2, s26, 0x31200000
	s_addc_u32 s3, s27, 0
	s_add_u32 s62, s26, 0x31210000
	v_writelane_b32 v254, s0, 10
	s_addc_u32 s63, s27, 0
	v_readlane_b32 s0, v249, 28
	s_cmp_lt_i32 s0, 64
	s_cselect_b64 s[0:1], -1, 0
	v_writelane_b32 v254, s0, 11
	s_nop 1
	v_writelane_b32 v254, s1, 12
	v_readlane_b32 s0, v249, 28
	s_and_b32 s0, s0, -4
	s_cmp_eq_u32 s0, 64
	s_cselect_b64 s[0:1], -1, 0
	v_writelane_b32 v254, s0, 13
	s_nop 1
	v_writelane_b32 v254, s1, 14
	v_readlane_b32 s0, v249, 28
	s_add_u32 s30, s0, 0xffffffc4
	s_addc_u32 s31, 0, -1
	s_mul_hi_u32 s0, s30, 0xc000
	s_mul_i32 s1, s31, 0xc000
	s_add_i32 s0, s0, s1
	s_mul_i32 s1, s30, 0xc000
	s_add_u32 s1, s26, s1
	s_addc_u32 s0, s27, s0
	s_add_u32 s28, s1, 0x106000
	s_addc_u32 s29, s0, 0
	v_writelane_b32 v254, s28, 15
	s_add_u32 s0, s26, 0x3b390000
	s_addc_u32 s1, s27, 0
	v_writelane_b32 v254, s29, 16
	v_writelane_b32 v254, s0, 17
	s_lshl_b64 s[30:31], s[30:31], 6
	s_nop 0
	v_writelane_b32 v254, s1, 18
	v_writelane_b32 v254, s7, 19
	s_add_u32 s0, s7, s30
	v_writelane_b32 v254, s43, 20
	s_addc_u32 s1, s43, s31
	v_writelane_b32 v254, s0, 21
	s_add_u32 s52, s26, 0x35300000
	s_addc_u32 s53, s27, 0
	v_writelane_b32 v254, s1, 22
	v_readlane_b32 s0, v249, 28
	s_cmpk_lt_i32 s0, 0x200
	s_cselect_b64 s[0:1], -1, 0
	v_writelane_b32 v254, s0, 23
	s_mov_b32 s31, s33
	s_mul_i32 s43, s58, 6
	v_writelane_b32 v254, s1, 24
	v_readlane_b32 s0, v249, 28
	s_lshl_b32 s0, s0, 6
	v_readlane_b32 s1, v249, 28
	s_and_b32 s0, s0, 0x1c0
	s_ashr_i32 s1, s1, 3
	s_add_i32 s0, s0, s1
	s_bfe_u32 s30, s1, 0x30002
	s_ashr_i32 s0, s0, 5
	s_and_b32 s28, s1, 3
	s_lshl_b32 s1, s0, 2
	s_lshl_b32 s33, s30, 20
	s_or_b32 s29, s1, s28
	v_writelane_b32 v254, s33, 25
	v_writelane_b32 v254, s29, 26
	s_lshl_b32 s29, s29, 8
	s_ashr_i32 s1, s0, 31
	v_writelane_b32 v254, s29, 27
	s_bitset1_b32 s29, 7
	v_writelane_b32 v254, s29, 28
	s_lshl_b64 s[74:75], s[0:1], 23
	v_writelane_b32 v254, s74, 29
	s_mov_b32 s7, 0x42b17218
	s_nop 0
	v_writelane_b32 v254, s75, 30
	s_add_u32 s74, s26, 0x24400080
	s_addc_u32 s75, s27, 0
	v_writelane_b32 v254, s74, 31
	s_lshl_b32 s33, s28, 19
	s_lshl_b64 s[28:29], s[0:1], 21
	v_writelane_b32 v254, s75, 32
	s_add_u32 s28, s52, s28
	v_writelane_b32 v254, s52, 33
	s_addc_u32 s29, s53, s29
	s_add_u32 s28, s28, s33
	v_writelane_b32 v254, s53, 34
	s_addc_u32 s29, s29, 0
	v_writelane_b32 v254, s28, 35
	s_lshl_b64 s[0:1], s[0:1], 22
	v_readlane_b32 s52, v249, 57
	v_writelane_b32 v254, s29, 36
	v_writelane_b32 v254, s0, 37
	v_readlane_b32 s53, v249, 58
	s_nop 0
	v_writelane_b32 v254, s1, 38
	v_writelane_b32 v254, s30, 39
	s_lshl_b32 s0, s30, 19
	v_writelane_b32 v254, s0, 40
	v_readlane_b32 s0, v249, 28
	s_cmpk_lt_i32 s0, 0x1a0
	s_cselect_b64 s[0:1], -1, 0
	v_writelane_b32 v254, s0, 41
	v_readlane_b32 s30, v249, 28
	s_nop 0
	v_writelane_b32 v254, s1, 42
	s_and_b64 s[0:1], s[0:1], exec
	v_readlane_b32 s0, v250, 58
	s_cselect_b32 s0, s4, s0
	v_readlane_b32 s1, v251, 0
	v_writelane_b32 v254, s0, 43
	v_readlane_b32 s0, v250, 59
	s_cselect_b32 s0, s1, s0
	v_readlane_b32 s4, v252, 37
	v_writelane_b32 v254, s0, 44
	v_readlane_b32 s0, v252, 24
	v_readlane_b32 s1, v252, 25
	s_and_b64 s[0:1], s[0:1], exec
	v_readlane_b32 s0, v252, 31
	v_readlane_b32 s1, v252, 38
	s_cselect_b32 s1, s1, s0
	v_readlane_b32 s0, v252, 30
	s_cselect_b32 s0, s4, s0
	v_readlane_b32 s4, v252, 39
	v_writelane_b32 v254, s0, 45
	v_writelane_b32 v251, s54, 0
	s_nop 0
	v_writelane_b32 v254, s1, 46
	v_readlane_b32 s0, v252, 35
	v_readlane_b32 s1, v252, 40
	s_cselect_b32 s1, s1, s0
	v_readlane_b32 s0, v252, 33
	s_cselect_b32 s0, s4, s0
	s_movk_i32 s4, 0x400
	v_writelane_b32 v254, s0, 47
	v_writelane_b32 v251, s55, 1
	s_nop 0
	v_writelane_b32 v254, s1, 48
	s_cselect_b32 s0, 0x800, s4
	v_writelane_b32 v254, s0, 49
	s_cselect_b32 s0, s4, 0x800
	v_writelane_b32 v254, s0, 50
	s_nop 1
	v_writelane_b32 v254, s1, 51
	v_readlane_b32 s0, v252, 49
	s_cmp_lt_u32 s0, 4
	s_cselect_b32 s0, s64, s5
	s_cselect_b32 s1, 0, s22
	s_cselect_b32 s5, s59, s15
	s_cselect_b32 s22, s23, s14
	s_lshl_b64 s[0:1], s[0:1], 12
	s_add_u32 s0, s22, s0
	s_addc_u32 s1, s5, s1
	s_lshl_b32 s5, s34, 1
	s_add_u32 s0, s0, s5
	s_addc_u32 s1, s1, 0
	v_writelane_b32 v254, s0, 52
	s_nop 1
	v_writelane_b32 v254, s1, 53
	v_readlane_b32 s0, v252, 50
	v_readlane_b32 s1, v252, 51
	s_and_b64 s[0:1], s[0:1], exec
	v_readlane_b32 s0, v252, 58
	s_cselect_b32 s1, s70, s35
	s_cselect_b32 s0, s0, s79
	v_writelane_b32 v254, s0, 54
	s_nop 1
	v_writelane_b32 v254, s1, 55
	v_readlane_b32 s0, v252, 57
	s_cselect_b32 s1, s76, s0
	v_readlane_b32 s0, v252, 56
	s_cselect_b32 s0, s71, s0
	s_nop 0
; __global__ void __launch_bounds__(512, 2) mk_fwd(Params p) {
;     ...
;     const int lo = p.ph_lo, hi = p.ph_hi;
;     XcdBarrier bar; bar.bar = (unsigned*)(p.ws + WS_CTL); bar.x = 0; bar.st = misc + 8; bar.gsz = (unsigned)G;
;     if (hi - lo > 1) bar = xcd_barrier_post((unsigned*)(p.ws + WS_CTL), misc + 8, (unsigned)G);
;     const bool split_ok = (G == 256) && (hi - lo > 1);
;     XcdBarrier bar2; bar2.bar = (unsigned*)(p.ws + WS_CTL) + 4096; bar2.x = 0; bar2.st = misc + 12; bar2.gsz = (unsigned)MIX_GW;
;     if (split_ok && bx < MIX_GW) bar2 = xcd_barrier_post((unsigned*)(p.ws + WS_CTL) + 4096, misc + 12, (unsigned)MIX_GW);
;     ...
;     if (IN(0)) { if (EN(0)) REP(0) ph_mod(p, lds); if (EN(1)) REP(1) ph_tables(p, lds); if (EN(2)) REP(2) { if (G == 256) { if (bx >= 192) ph_weights(p, lds, 0, 240, bx - 192, 64); } else ph_weights(p, lds, 0, 6880, bx, G); } }
;     SEAM(0);
;     for (int l = 0; l < 2; ++l) {
;         const int pb = 1 + 10 * l;
;         const char* H = (const char*)(p.ws + WS_H);
;         if (EN(3) && IN(pb + 0)) REP(3) { if (G == 256 && !split_ok && bx < 4) ph_rbias(p, l, bx); if (l == 0) ph_norm1_l0(p); else ph_norm1(p, 1, lds); }
;         SEAM(pb + 0);
;         const bool split = split_ok && l == 0 && EN(2);
;         const int vG = split ? MIX_GW : G;
;         if (EN(4) && IN(pb + 1) && (!split || bx < MIX_GW)) REP(4) {
;             SchedProj S{H, (const char*)(p.ws + WS_WIN) + (size_t)l * NPROJ * 2048 * 2, (const char*)(p.ws + WS_WPQ) + (size_t)l * 512 * 2048 * 2, vG, bx};
;             EpiProj E{(bf16_t*)(p.ws + WS_PROJ), (bf16_t*)(p.ws + WS_PQT), (const float*)(p.ws + WS_ROPE), (const float*)(p.ws + WS_ROPE) + NT * 8};
;             pg8::gemm_phase<EpiProj, SchedProj>(lds, 2048, 2048, 2048, S, E);
;         }
;         if (split) { if (bx < MIX_GW && IN(pb + 1) && IN(pb + 2)) xcd_barrier(bar2); } else SEAM(pb + 1);
;         if (IN(pb + 2)) {
;             if (!split || bx < MIX_GW) {
;                 if (EN(5)) REP(5) ph_fft(p, lds, bx, vG);
;                 __syncthreads();
;                 if (EN(8)) REP(8) ph_mixers(p, l, lds, bx, vG);
;             } else { if (bx - MIX_GW < 4) ph_rbias(p, 0, bx - MIX_GW); ph_weights(p, lds, 240, 6880, bx - MIX_GW, G - MIX_GW); }
;         }
;         SEAM(pb + 2);
;         if (EN(9) && IN(pb + 3)) REP(9) { ph_merge(p, l, lds); }
;         SEAM(pb + 3);
	v_writelane_b32 v254, s0, 56
	s_nop 1
	v_writelane_b32 v254, s1, 57
	s_cselect_b32 s0, 0x800, s4
	v_writelane_b32 v254, s0, 58
	s_cselect_b32 s0, s4, 0x800
	v_writelane_b32 v254, s0, 59
	s_cmp_lt_u32 s69, 4
	s_cselect_b32 s5, s59, s15
	v_writelane_b32 v254, s1, 60
	s_cselect_b32 s0, s65, s78
	s_cselect_b32 s1, 0, s68
	s_cselect_b32 s22, s23, s14
	s_lshl_b64 s[0:1], s[0:1], 12
	s_add_u32 s0, s22, s0
	s_addc_u32 s1, s5, s1
	s_lshl_b32 s5, s77, 1
	s_add_u32 s0, s0, s5
	s_addc_u32 s1, s1, 0
	v_writelane_b32 v254, s0, 61
	s_mov_b64 s[64:65], 0x80
	s_nop 0
	v_writelane_b32 v254, s1, 62
	s_and_b64 s[0:1], s[66:67], exec
	s_cselect_b32 s1, s57, s87
	s_cselect_b32 s0, s37, s86
	v_writelane_b32 v254, s0, 63
	s_nop 1
	v_writelane_b32 v255, s1, 0
	s_cselect_b32 s1, s89, s36
	s_cselect_b32 s0, s88, s6
	v_writelane_b32 v255, s0, 1
	s_movk_i32 s6, 0x1a00
	s_nop 0
	v_writelane_b32 v255, s1, 2
	s_cselect_b32 s0, 0x800, s4
	v_writelane_b32 v255, s0, 3
	s_cselect_b32 s0, s4, 0x800
	v_writelane_b32 v255, s0, 4
	s_cmp_lt_i32 s90, 4
	s_cselect_b32 s5, s9, s15
	v_writelane_b32 v255, s1, 5
	s_cselect_b32 s0, s12, s91
	s_cselect_b32 s1, s13, 0
	s_cselect_b32 s12, s8, s14
	s_lshl_b64 s[0:1], s[0:1], 12
	s_add_u32 s12, s12, s0
	s_addc_u32 s5, s5, s1
	s_lshl_b64 s[0:1], s[10:11], 1
	s_add_u32 s0, s12, s0
	s_addc_u32 s1, s5, s1
	v_writelane_b32 v255, s0, 6
	s_nop 1
	v_writelane_b32 v255, s1, 7
	s_and_b64 s[0:1], s[38:39], exec
	s_cselect_b32 s1, s95, s41
	s_cselect_b32 s0, s94, s40
	v_writelane_b32 v255, s0, 8
	s_nop 1
	v_writelane_b32 v255, s1, 9
	s_cselect_b32 s1, s97, s49
	s_cselect_b32 s0, s96, s48
	v_writelane_b32 v255, s0, 10
	s_nop 1
	v_writelane_b32 v255, s1, 11
	s_cselect_b32 s0, 0x800, s4
	v_writelane_b32 v255, s0, 12
	s_cselect_b32 s0, s4, 0x800
	v_writelane_b32 v255, s0, 13
	s_cmp_lt_i32 s56, 4
	s_cselect_b32 s4, s9, s15
	v_writelane_b32 v255, s1, 14
	s_cselect_b32 s0, s20, s60
	s_cselect_b32 s1, s21, 0
	v_writelane_b32 v252, s14, 31
	s_cselect_b32 s5, s8, s14
	s_lshl_b64 s[0:1], s[0:1], 12
	s_add_u32 s5, s5, s0
	s_addc_u32 s4, s4, s1
	s_lshl_b64 s[0:1], s[18:19], 1
	s_add_u32 s0, s5, s0
	s_addc_u32 s1, s4, s1
	v_writelane_b32 v255, s0, 15
	v_writelane_b32 v252, s15, 32
	v_readlane_b32 s20, v250, 4
	v_writelane_b32 v255, s1, 16
	v_readlane_b32 s0, v249, 52
	s_add_i32 s0, s0, s42
	s_ashr_i32 s1, s0, 31
	s_lshr_b32 s1, s1, 26
	s_add_i32 s1, s0, s1
	s_and_b32 s4, s1, 0xffc0
	s_sub_i32 s0, s0, s4
	s_bfe_i32 s4, s0, 0x80000
	s_bfe_u32 s4, s4, 0x3000c
	s_add_i32 s4, s0, s4
	s_and_b32 s5, s4, 0xf8
	s_sub_i32 s0, s0, s5
	s_ashr_i32 s1, s1, 6
	s_bfe_i32 s4, s4, 0x80000
	s_lshl_b32 s1, s1, 3
	s_sext_i32_i16 s4, s4
	s_sext_i32_i8 s0, s0
	s_add_i32 s8, s1, s0
	s_ashr_i32 s0, s4, 3
	v_writelane_b32 v255, s0, 17
	s_lshr_b32 s0, s4, 3
	s_mov_b32 s4, s8
	s_ashr_i32 s9, s8, 31
	v_writelane_b32 v255, s4, 18
	s_mul_i32 s42, s58, 3
	v_readlane_b32 s14, v250, 49
	v_writelane_b32 v255, s5, 19
	s_lshl_b64 s[4:5], s[8:9], 20
	s_add_u32 s4, s72, s4
	v_writelane_b32 v255, s72, 20
	s_addc_u32 s5, s73, s5
	s_bfe_i64 s[0:1], s[0:1], 0x100000
	v_writelane_b32 v255, s73, 21
	v_writelane_b32 v255, s4, 22
	s_lshl_b64 s[0:1], s[0:1], 20
	v_readlane_b32 s18, v249, 60
	v_writelane_b32 v255, s5, 23
	v_writelane_b32 v255, s0, 24
	s_add_i32 s4, s43, 0xfffffde1
	v_readlane_b32 s21, v249, 59
	v_writelane_b32 v255, s1, 25
	s_add_i32 s0, s30, s42
	s_lshl_b32 s0, s0, 1
	s_addk_i32 s0, 0xfde0
	v_writelane_b32 v255, s0, 26
	s_mul_i32 s0, s58, 0x300
	s_add_i32 s1, s0, 0xfffef000
	v_writelane_b32 v255, s1, 27
	s_add_i32 s0, s0, 0xfffef080
	v_writelane_b32 v255, s0, 28
	s_add_i32 s0, s43, 0xffffeb00
	v_writelane_b32 v255, s0, 29
	s_add_i32 s0, s43, 0xfffffb00
	v_writelane_b32 v255, s0, 30
	s_add_i32 s0, s43, 0xfffffde0
	v_writelane_b32 v255, s0, 31
	s_add_i32 s0, s43, 0xffffeb01
	v_writelane_b32 v255, s0, 32
	s_add_i32 s0, s43, 0xfffffb01
	v_writelane_b32 v255, s0, 33
	s_mul_i32 s0, s58, 0x60
	s_add_i32 s1, s0, 0xffffb000
	v_writelane_b32 v255, s1, 34
	s_addk_i32 s0, 0xb010
	v_writelane_b32 v255, s0, 35
	s_mul_i32 s0, s58, 48
	s_add_i32 s1, s0, 0xffff5800
	v_writelane_b32 v255, s1, 36
	s_add_i32 s1, s0, 0xffffef00
	v_writelane_b32 v255, s1, 37
	s_add_i32 s1, s0, 0xffff5808
	v_writelane_b32 v255, s1, 38
	s_addk_i32 s0, 0xef08
	v_writelane_b32 v255, s0, 39
	s_add_i32 s0, s42, 0xfffffef0
	v_writelane_b32 v252, s0, 37
	s_lshl_b32 s0, s58, 1
	s_add_i32 s1, s30, s0
	s_lshl_b32 s1, s1, 1
	s_addk_i32 s1, 0xfee0
	v_writelane_b32 v255, s1, 40
	s_lshl_b32 s1, s58, 9
	s_add_i32 s5, s1, 0xffff0000
	v_writelane_b32 v252, s5, 38
	s_add_i32 s5, s1, 0xffff7000
	v_writelane_b32 v255, s5, 41
	s_add_i32 s1, s1, 0xffff7080
	v_writelane_b32 v255, s1, 42
	s_lshl_b32 s1, s58, 2
	s_add_i32 s5, s1, 0xfffffe00
	v_writelane_b32 v252, s5, 39
	s_add_i32 s5, s1, 0xffffec00
	v_writelane_b32 v255, s5, 43
	s_add_i32 s5, s1, 0xfffffc00
	v_writelane_b32 v255, s5, 44
	s_add_i32 s5, s1, 0xfffffee0
	s_add_i32 s8, s1, 0xffffec01
	v_writelane_b32 v252, s5, 50
	s_add_i32 s5, s1, 0xfffffee1
	v_writelane_b32 v255, s8, 45
	s_addk_i32 s1, 0xfc01
	v_writelane_b32 v255, s1, 46
	s_lshl_b32 s1, s58, 6
	s_add_i32 s8, s1, 0xffffe000
	v_writelane_b32 v252, s8, 40
	s_add_i32 s8, s1, 0xffffc000
	v_writelane_b32 v255, s8, 47
	s_addk_i32 s1, 0xc010
	s_addk_i32 s0, 0xff70
	v_writelane_b32 v255, s1, 48
	v_writelane_b32 v252, s0, 30
	s_lshl_b32 s0, s30, 4
	v_writelane_b32 v255, s0, 49
	s_add_i32 s0, s20, 0xfffff000
	v_writelane_b32 v252, s0, 49
	s_lshl_b32 s0, s30, 8
	v_writelane_b32 v255, s0, 50
	v_writelane_b32 v255, s4, 51
	s_add_i32 s0, s4, s44
	v_writelane_b32 v255, s0, 52
	s_add_i32 s0, s20, 0xffff6000
	v_writelane_b32 v255, s0, 53
	s_add_i32 s0, s20, 0xfffff700
	v_writelane_b32 v255, s0, 54
	s_add_i32 s0, s20, 0xffff6008
	v_writelane_b32 v255, s0, 55
	v_writelane_b32 v255, s44, 56
	s_add_i32 s0, s5, s44
	v_writelane_b32 v255, s0, 57
	s_add_i32 s0, s20, 0xfffff708
	v_writelane_b32 v255, s0, 58
	s_add_i32 s0, 0, 0x27f20
	v_writelane_b32 v252, s0, 56
	s_add_i32 s0, 0, 0x27f24
	v_writelane_b32 v252, s0, 57
	v_cmp_eq_u32_e64 s[8:9], 0, v0
	s_add_i32 s0, 0, 0x27f30
	v_writelane_b32 v255, s0, 59
	v_writelane_b32 v252, s8, 33
	s_add_i32 s0, 0, 0x27f34
	v_readlane_b32 s15, v250, 50
	v_writelane_b32 v252, s9, 34
	v_writelane_b32 v252, s46, 24
	v_readlane_b32 s19, v249, 61
	v_writelane_b32 v250, s5, 58
	s_mov_b32 s5, 0xf800000
	s_movk_i32 s43, 0x4000
	v_writelane_b32 v255, s0, 60
	s_mov_b32 s1, 0x5040100
	s_mov_b32 s0, s61
	v_writelane_b32 v252, s47, 25
	s_branch .LBB0_333

; #define REP(k) _Pragma("unroll") for (int rep_ = 0; rep_ < 1 + (int)(((REP_MASK) >> (k)) & 1u); ++rep_)
; __global__ void __launch_bounds__(512, 2) mk_fwd(Params p) {
;     ...
;         const bool split = split_ok && l == 0 && EN(2);
;         const int vG = split ? MIX_GW : G;
;         if (EN(4) && IN(pb + 1) && (!split || bx < MIX_GW)) REP(4) {
;             SchedProj S{H, (const char*)(p.ws + WS_WIN) + (size_t)l * NPROJ * 2048 * 2, (const char*)(p.ws + WS_WPQ) + (size_t)l * 512 * 2048 * 2, vG, bx};
;             EpiProj E{(bf16_t*)(p.ws + WS_PROJ), (bf16_t*)(p.ws + WS_PQT), (const float*)(p.ws + WS_ROPE), (const float*)(p.ws + WS_ROPE) + NT * 8};
;             pg8::gemm_phase<EpiProj, SchedProj>(lds, 2048, 2048, 2048, S, E);
.LBB0_413:
	v_readlane_b32 s8, v249, 10
	v_readlane_b32 s10, v249, 49
	v_readlane_b32 s9, v249, 11
	v_readlane_b32 s11, v249, 50
	s_and_b64 s[10:11], s[8:9], s[10:11]
	s_and_b64 s[8:9], s[10:11], exec
	v_readlane_b32 s8, v249, 8
	s_cselect_b32 s29, 0xa0, s58
	v_readlane_b32 s9, v249, 9
	s_cmp_le_i32 s8, s4
	s_cselect_b64 s[36:37], -1, 0
	s_cmp_lt_i32 s4, s9
	s_cselect_b64 s[8:9], -1, 0
	s_and_b64 s[40:41], s[8:9], s[36:37]
	v_readlane_b32 s8, v249, 47
	v_writelane_b32 v252, s10, 58
	s_xor_b64 s[44:45], s[10:11], -1
	v_readlane_b32 s9, v249, 48
	s_or_b64 s[56:57], s[8:9], s[44:45]
	s_and_b64 s[8:9], s[56:57], s[40:41]
	v_writelane_b32 v252, s11, 59
	s_andn2_b64 vcc, exec, s[8:9]
	s_cbranch_vccnz .LBB0_670
	v_readlane_b32 s10, v250, 59
	v_readlane_b32 s11, v250, 60
	s_mul_i32 s4, s10, 0xd00000
	v_readlane_b32 s8, v252, 31
	s_mov_b32 s0, s10
	s_mov_b32 s11, s61
	v_readlane_b32 s9, v252, 32
	s_add_u32 s95, s8, s4
	v_writelane_b32 v250, s0, 59
	s_addc_u32 s96, s9, 0
	s_lshl_b64 s[8:9], s[10:11], 21
	v_writelane_b32 v250, s1, 60
	v_readlane_b32 s0, v253, 16
	s_add_u32 s97, s0, s8
	v_readlane_b32 s0, v253, 17
	s_addc_u32 s42, s0, s9
	v_readlane_b32 s8, v250, 56
	v_readlane_b32 s9, v250, 57
	s_waitcnt vmcnt(0)
	v_mov_b32_e32 v10, v0
	s_andn2_b64 vcc, exec, s[8:9]
	v_cndmask_b32_e64 v1, 0, 1, s[8:9]
	v_cmp_ne_u32_e64 s[34:35], 1, v1
	v_readfirstlane_b32 s8, v10
	s_cbranch_vccnz .LBB0_416
	v_readlane_b32 s10, v251, 4
	v_readlane_b32 s11, v251, 5
	s_add_u32 s4, s95, s10
	s_addc_u32 s9, s96, s11
	v_readlane_b32 s0, v250, 61
	s_add_u32 s22, s97, s0
	v_readlane_b32 s10, v254, 41
	s_addc_u32 s23, s42, 0
	v_readlane_b32 s11, v254, 42
	s_and_b64 s[10:11], s[10:11], exec
	v_readlane_b32 s0, v250, 63
	s_cselect_b32 s13, s9, s0
	v_readlane_b32 s0, v250, 62
	s_cselect_b32 s12, s4, s0
	v_readlane_b32 s0, v251, 3
	s_cselect_b32 s67, s0, s23
	v_readlane_b32 s0, v251, 2
	s_cselect_b32 s66, s0, s22
	v_readlane_b32 s39, v254, 44
	v_readlane_b32 s9, v254, 43

; __device__ __forceinline__ unsigned xb_ld(unsigned* p)              { return __hip_atomic_load(p, __ATOMIC_RELAXED, __HIP_MEMORY_SCOPE_AGENT); }
; __device__ __forceinline__ void xcd_barrier_complete(unsigned* bar, unsigned x, unsigned& nloc, unsigned& nx, const unsigned G) {
;     unsigned sum, cnt, mine, sp = 0u;
;     for (;;) {
;         sum = 0u; cnt = 0u; mine = 0u;
; #pragma unroll
;         for (unsigned j = 0; j < 16; ++j) { const unsigned c = xb_ld(&bar[XB_XCNT(j)]); sum += c; cnt += (c > 0u) ? 1u : 0u; mine = (j == x) ? c : mine; }
;         if (sum == G) break;
;         __builtin_amdgcn_s_sleep(1);
;         if ((++sp & 255u) == 0u) { if (xb_ld(&bar[XB_TMO])) break; if (sp > XB_SPIN_CAP) { atomicAdd(&bar[XB_TMO], 1u); break; } }
;     }
;     nloc = mine > 0u ? mine : 1u; nx = cnt > 0u ? cnt : 1u;
; }
.LBB0_690:
	v_readlane_b32 s8, v251, 10
	v_readlane_b32 s9, v251, 11
	s_mov_b64 s[34:35], -1
	s_mov_b64 s[38:39], -1
	s_nop 2
	global_load_dword v1, v195, s[8:9] sc1
	v_readlane_b32 s8, v251, 12
	v_readlane_b32 s9, v251, 13
	s_waitcnt lgkmcnt(0)
	s_nop 3
	global_load_dword v2, v195, s[8:9] sc1
	v_readlane_b32 s8, v251, 14
	v_readlane_b32 s9, v251, 15
	s_waitcnt vmcnt(0)
	v_add_u32_e32 v17, v2, v1
	s_nop 2
	global_load_dword v3, v195, s[8:9] sc1
	v_readlane_b32 s8, v251, 16
	v_readlane_b32 s9, v251, 17
	s_waitcnt vmcnt(0)
	v_add_u32_e32 v17, v17, v3
	s_nop 2
	global_load_dword v4, v195, s[8:9] sc1
	v_readlane_b32 s8, v251, 18
	v_readlane_b32 s9, v251, 19
	s_waitcnt vmcnt(0)
	v_add_u32_e32 v17, v17, v4
	s_nop 2
	global_load_dword v5, v195, s[8:9] sc1
	v_readlane_b32 s8, v251, 20
	v_readlane_b32 s9, v251, 21
	s_waitcnt vmcnt(0)
	v_add_u32_e32 v17, v17, v5
	s_nop 2
	global_load_dword v6, v195, s[8:9] sc1
	v_readlane_b32 s8, v251, 22
	v_readlane_b32 s9, v251, 23
	s_waitcnt vmcnt(0)
	v_add_u32_e32 v17, v17, v6
	s_nop 2
	global_load_dword v7, v195, s[8:9] sc1
	v_readlane_b32 s8, v251, 24
	v_readlane_b32 s9, v251, 25
	s_waitcnt vmcnt(0)
	v_add_u32_e32 v17, v17, v7
	s_nop 2
	global_load_dword v8, v195, s[8:9] sc1
	v_readlane_b32 s8, v251, 26
	v_readlane_b32 s9, v251, 27
	s_waitcnt vmcnt(0)
	v_add_u32_e32 v17, v17, v8
	s_nop 2
	global_load_dword v9, v195, s[8:9] sc1
	v_readlane_b32 s8, v251, 28
	v_readlane_b32 s9, v251, 29
	s_waitcnt vmcnt(0)
	v_add_u32_e32 v17, v17, v9
	s_nop 2
	global_load_dword v10, v195, s[8:9] sc1
	v_readlane_b32 s8, v251, 30
	v_readlane_b32 s9, v251, 31
	s_waitcnt vmcnt(0)
	v_add_u32_e32 v17, v17, v10
	s_nop 2
	global_load_dword v11, v195, s[8:9] sc1
	v_readlane_b32 s8, v251, 32
	v_readlane_b32 s9, v251, 33
	s_waitcnt vmcnt(0)
	v_add_u32_e32 v17, v17, v11
	s_nop 2
	global_load_dword v12, v195, s[8:9] sc1
	v_readlane_b32 s8, v251, 34
	v_readlane_b32 s9, v251, 35
	s_waitcnt vmcnt(0)
	v_add_u32_e32 v17, v17, v12
	s_nop 2
	global_load_dword v13, v195, s[8:9] sc1
	v_readlane_b32 s8, v251, 36
	v_readlane_b32 s9, v251, 37
	s_waitcnt vmcnt(0)
	v_add_u32_e32 v17, v17, v13
	s_nop 2
	global_load_dword v14, v195, s[8:9] sc1
	v_readlane_b32 s8, v251, 38
	v_readlane_b32 s9, v251, 39
	s_waitcnt vmcnt(0)
	v_add_u32_e32 v17, v17, v14
	s_nop 2
	global_load_dword v15, v195, s[8:9] sc1
	v_readlane_b32 s8, v251, 40
	v_readlane_b32 s9, v251, 41
	s_waitcnt vmcnt(0)
	v_add_u32_e32 v17, v17, v15
	s_nop 2
	global_load_dword v16, v195, s[8:9] sc1
	s_movk_i32 s8, 0xa0
	s_waitcnt vmcnt(0)
	v_add_u32_e32 v17, v17, v16
	v_cmp_eq_u32_e32 vcc, s8, v17
	s_cbranch_vccnz .LBB0_689
	s_and_b32 s8, s4, 0xff
	s_cmp_eq_u32 s8, 0
	s_mov_b64 s[40:41], -1
	s_sleep 1
	s_cbranch_scc1 .LBB0_694
	s_and_b64 vcc, exec, s[40:41]
	s_cbranch_vccz .LBB0_689

; __device__ __forceinline__ bool tdecode(const Params& p, int it, TDesc& d) {
;     if (it >= 2 * 6880) return false;
;     const int l = it / 6880; int r = it % 6880;
;     d.ksc = nullptr;
;     if (r < 480) { const int kt = r / 30, nt = r % 30;
;         d.src = p.in[6] + ((size_t)l * 2048 + kt * 128) * DIN + nt * 128; d.lds_ = DIN;
;         d.dst = (nt < 4 ? (bf16_t*)(p.ws + WS_WPQ) + ((size_t)l * 512 + nt * 128) * 2048 : (bf16_t*)(p.ws + WS_WIN) + ((size_t)l * NPROJ + (nt - 4) * 128) * 2048) + kt * 128; d.ldd = 2048; return true; }
;     r -= 480;
;     if (r < 256) { const int kt = r / 16, nt = r % 16;
;         d.src = p.in[13] + ((size_t)l * 2048 + kt * 128) * 2048 + nt * 128; d.lds_ = 2048; d.ksc = p.in[12] + (size_t)l * 2048 + kt * 128;
;         d.dst = (bf16_t*)(p.ws + WS_WOUT) + ((size_t)l * 2048 + nt * 128) * 2048 + kt * 128; d.ldd = 2048; return true; }
;     r -= 256;
;     if (r < 4096) { const int isup = r / 2048, r2 = r % 2048, e = r2 / 128, kt = (r2 % 128) / 8, nt = r2 % 8;
;         d.src = p.in[isup ? 17 : 16] + (((size_t)l * 16 + e) * 2048 + kt * 128) * 1024 + nt * 128; d.lds_ = 1024;
;         d.dst = (bf16_t*)(p.ws + WS_WGU) + (((size_t)l * 16 + e) * 2048 + nt * 256 + isup * 128) * 2048 + kt * 128; d.ldd = 2048; return true; }
;     r -= 4096;
;     { const int e = r / 128, kt = (r % 128) / 16, nt = r % 16;
;         d.src = p.in[18] + (((size_t)l * 16 + e) * 1024 + kt * 128) * 2048 + nt * 128; d.lds_ = 2048;
;         d.dst = (bf16_t*)(p.ws + WS_WD) + (((size_t)l * 16 + e) * 2048 + nt * 128) * 1024 + kt * 128; d.ldd = 1024; return true; }
; }
; __device__ __forceinline__ void ph_weights(const Params& p, LAS unsigned char* lds, const int p0, const int p1, const int wi, const int wn) {
;     ...
;     int pi = p0 + wi; bool hA, hB;
;     PW_LOAD(pi, dA0, dA1, a0, a1, hA);
;     PW_LOAD(pi + wn, dB0, dB1, b0, b1, hB);
.LBB0_779:
	v_writelane_b32 v255, s29, 61
	s_waitcnt lgkmcnt(0)
	v_and_b32_e32 v166, 31, v0
	v_lshrrev_b32_e32 v167, 5, v0
	v_lshlrev_b32_e32 v168, 1, v167
	v_lshlrev_b32_e32 v169, 4, v166
	v_lshlrev_b32_e32 v170, 3, v167
	v_lshrrev_b32_e32 v1, 2, v167
	v_lshlrev_b32_e32 v1, 4, v1
	v_xor_b32_e32 v1, v169, v1
	v_lshl_add_u32 v154, v167, 9, v1
	v_xor_b32_e32 v155, 64, v154
	v_xor_b32_e32 v156, 0x80, v154
	v_xor_b32_e32 v157, 0xc0, v154
	v_and_b32_e32 v171, 15, v0
	v_lshrrev_b32_e32 v175, 4, v0
	v_lshlrev_b32_e32 v1, 2, v171
	v_xor_b32_e32 v1, v175, v1
	v_lshlrev_b32_e32 v174, 11, v171
	v_lshl_add_u32 v162, v1, 2, v174
	v_xor_b32_e32 v163, 0x80, v162
	v_xor_b32_e32 v164, 0x100, v162
	v_xor_b32_e32 v165, 0x180, v162
	v_lshlrev_b32_e32 v176, 4, v171
	v_add_u32_e32 v158, 0x10000, v154
	v_add_u32_e32 v159, 0x10000, v155
	v_add_u32_e32 v160, 0x10000, v156
	v_add_u32_e32 v161, 0x10000, v157
	v_add_u32_e32 v130, 0x10000, v162
	v_add_u32_e32 v131, 0x10000, v163
	v_add_u32_e32 v132, 0x10000, v164
	v_add_u32_e32 v133, 0x10000, v165
	v_readlane_b32 s0, v249, 28
	s_nop 3
	s_add_u32 s0, s0, 80
	s_mov_b32 s9, 3
	s_cmp_ge_u32 s0, 0xd70
	s_cselect_b32 s77, 1, 0
	s_mul_i32 s83, s77, 0xd70
	s_sub_u32 s78, s0, s83
	v_readlane_b32 s20, v249, 37
	v_readlane_b32 s21, v249, 38
	s_mov_b32 s29, 0
	s_cmpk_lt_u32 s78, 0xf0
	s_cbranch_scc1 .Lcv_win_A1
	s_cmpk_lt_u32 s78, 0x170
	s_cbranch_scc1 .Lcv_wout_A1
	s_cmpk_lt_u32 s78, 0x970
	s_cbranch_scc1 .Lcv_gu_A1
	s_sub_u32 s78, s78, 0x970
	s_lshr_b32 s83, s78, 6
	s_bfe_u32 s93, s78, 0x30003
	s_and_b32 s94, s78, 7
	s_mul_i32 s98, s77, 0x8000000
	s_lshl_b32 s95, s83, 23
	s_add_u32 s98, s98, s95
	s_lshl_b32 s95, s93, 20
	s_add_u32 s98, s98, s95
	s_lshl_b32 s95, s94, 10
	s_add_u32 s98, s98, s95
	s_mul_i32 s99, s77, 0x4000000
	s_add_u32 s99, s99, 0x14400000
	s_lshl_b32 s95, s83, 22
	s_add_u32 s99, s99, s95
	s_lshl_b32 s95, s94, 19
	s_add_u32 s99, s99, s95
	s_lshl_b32 s95, s93, 8
	s_add_u32 s99, s99, s95
	v_readlane_b32 s12, v249, 4
	v_readlane_b32 s13, v249, 5
	s_movk_i32 s22, 0x2000
	s_movk_i32 s23, 0x800
	s_mov_b32 s28, 0x40000
	s_branch .Lcv_fin_A1
.Lcv_gu_A1:
	s_sub_u32 s78, s78, 0x170
	s_lshr_b32 s83, s78, 10
	s_bfe_u32 s93, s78, 0x40006
	s_bfe_u32 s94, s78, 0x40002
	s_and_b32 s95, s78, 3
	s_mul_i32 s98, s77, 0x8000000
	s_lshl_b32 s78, s93, 23
	s_add_u32 s98, s98, s78
	s_mov_b32 s99, s98
	s_lshl_b32 s78, s94, 19
	s_add_u32 s98, s98, s78
	s_lshl_b32 s78, s95, 10
	s_add_u32 s98, s98, s78
	s_add_u32 s99, s99, 0x4400000
	s_lshl_b32 s78, s95, 21
	s_add_u32 s99, s99, s78
	s_lshl_b32 s78, s83, 19
	s_add_u32 s99, s99, s78
	s_lshl_b32 s78, s94, 8
	s_add_u32 s99, s99, s78
	s_cmp_eq_u32 s83, 0
	s_cbranch_scc0 .Lcv_up_A1
	v_readlane_b32 s12, v249, 0
	v_readlane_b32 s13, v249, 1
	s_branch .Lcv_gu2_A1
.Lcv_up_A1:
	v_readlane_b32 s12, v249, 2
	v_readlane_b32 s13, v249, 3
.Lcv_gu2_A1:
	s_movk_i32 s22, 0x1000
	s_movk_i32 s23, 0x1000
	s_mov_b32 s28, 0x100000
	s_branch .Lcv_fin_A1
.Lcv_wout_A1:
	s_sub_u32 s78, s78, 0xf0
	s_lshr_b32 s83, s78, 3
	s_and_b32 s93, s78, 7
	s_lshl_b32 s98, s77, 24
	s_lshl_b32 s95, s83, 20
	s_add_u32 s98, s98, s95
	s_lshl_b32 s95, s93, 10
	s_add_u32 s98, s98, s95
	s_lshl_b32 s99, s77, 23
	s_add_u32 s99, s99, 0x3400000
	s_lshl_b32 s95, s93, 20
	s_add_u32 s99, s99, s95
	s_lshl_b32 s95, s83, 8
	s_add_u32 s99, s99, s95
	s_lshl_b32 s94, s77, 13
	s_lshl_b32 s95, s83, 9
	s_add_u32 s94, s94, s95
	s_nop 3
	s_add_u32 s20, s20, s94
	s_addc_u32 s21, s21, 0
	v_readlane_b32 s12, v249, 39
	v_readlane_b32 s13, v249, 40
	s_movk_i32 s22, 0x2000
	s_movk_i32 s23, 0x1000
	s_mov_b32 s28, 0x80000
	s_mov_b32 s29, 1
	s_branch .Lcv_fin_A1
.Lcv_win_A1:
	s_mul_i32 s83, s78, 0x1112
	s_lshr_b32 s83, s83, 16
	s_mul_i32 s93, s83, 15
	s_sub_u32 s93, s78, s93
	s_mul_i32 s98, s77, 0x1e00000
	s_mul_i32 s95, s83, 0x1e0000
	s_add_u32 s98, s98, s95
	s_lshl_b32 s95, s93, 10
	s_add_u32 s98, s98, s95
	s_cmp_lt_u32 s93, 2
	s_cbranch_scc0 .Lcv_win2_A1
	s_lshl_b32 s99, s77, 21
	s_add_u32 s99, s99, 0x2c00000
	s_lshl_b32 s95, s93, 20
	s_add_u32 s99, s99, s95
	s_branch .Lcv_win3_A1
.Lcv_win2_A1:
	s_mul_i32 s99, s77, 0xd00000
	s_add_u32 s99, s99, 0x1200000
	s_sub_u32 s95, s93, 2
	s_lshl_b32 s95, s95, 20
	s_add_u32 s99, s99, s95
.Lcv_win3_A1:
	s_lshl_b32 s95, s83, 8
	s_add_u32 s99, s99, s95
	v_readlane_b32 s12, v249, 24
	v_readlane_b32 s13, v249, 25
	s_movk_i32 s22, 0x3c00
	s_movk_i32 s23, 0x1000
	s_mov_b32 s28, 0x80000
; __device__ __forceinline__ void ph_weights(const Params& p, LAS unsigned char* lds, const int p0, const int p1, const int wi, const int wn) {
;     ...
;     int pi = p0 + wi; bool hA, hB;
;     PW_LOAD(pi, dA0, dA1, a0, a1, hA);
;     PW_LOAD(pi + wn, dB0, dB1, b0, b1, hB);
.Lcv_fin_A1:
	s_nop 3
	s_add_u32 s12, s12, s98
	s_addc_u32 s13, s13, 0
	s_add_u32 s14, s26, s99
	s_addc_u32 s15, s27, 0
	v_mad_u32_u24 v177, v168, s22, v169
	s_mov_b64 s[88:89], s[12:13]
	s_add_u32 s90, s12, s22
	s_addc_u32 s91, s13, 0
	s_lshl_b32 s92, s22, 5
	global_load_dwordx2 v[138:139], v170, s[20:21]
	global_load_dwordx2 v[140:141], v170, s[20:21] offset:128
	global_load_dwordx2 v[142:143], v170, s[20:21] offset:256
	global_load_dwordx2 v[144:145], v170, s[20:21] offset:384
	global_load_dwordx4 v[2:5], v177, s[88:89] nt
	global_load_dwordx4 v[34:37], v177, s[88:89] offset:512 nt
	global_load_dwordx4 v[6:9], v177, s[90:91] nt
	global_load_dwordx4 v[38:41], v177, s[90:91] offset:512 nt
	s_add_u32 s88, s88, s92
	s_addc_u32 s89, s89, 0
	s_add_u32 s90, s90, s92
	s_addc_u32 s91, s91, 0
	global_load_dwordx4 v[10:13], v177, s[88:89] nt
	global_load_dwordx4 v[42:45], v177, s[88:89] offset:512 nt
	global_load_dwordx4 v[14:17], v177, s[90:91] nt
	global_load_dwordx4 v[46:49], v177, s[90:91] offset:512 nt
	s_add_u32 s88, s88, s92
	s_addc_u32 s89, s89, 0
	s_add_u32 s90, s90, s92
	s_addc_u32 s91, s91, 0
	global_load_dwordx4 v[18:21], v177, s[88:89] nt
	global_load_dwordx4 v[50:53], v177, s[88:89] offset:512 nt
	global_load_dwordx4 v[22:25], v177, s[90:91] nt
	global_load_dwordx4 v[54:57], v177, s[90:91] offset:512 nt
	s_add_u32 s88, s88, s92
	s_addc_u32 s89, s89, 0
	s_add_u32 s90, s90, s92
	s_addc_u32 s91, s91, 0
	global_load_dwordx4 v[26:29], v177, s[88:89] nt
	global_load_dwordx4 v[58:61], v177, s[88:89] offset:512 nt
	global_load_dwordx4 v[30:33], v177, s[90:91] nt
	global_load_dwordx4 v[62:65], v177, s[90:91] offset:512 nt
	global_load_dword v1, v170, s[20:21]
	global_load_dword v1, v170, s[20:21]
	global_load_dword v1, v170, s[20:21]
	global_load_dword v1, v170, s[20:21]
	global_load_dword v1, v170, s[20:21]
	global_load_dword v1, v170, s[20:21]
	global_load_dword v1, v170, s[20:21]
	global_load_dword v1, v170, s[20:21]
	s_add_u32 s86, s0, 96
	s_cmp_ge_u32 s86, 0xd70
	s_cselect_b32 s77, 1, 0
	s_mul_i32 s83, s77, 0xd70
	s_sub_u32 s78, s86, s83
	v_readlane_b32 s36, v249, 37
	v_readlane_b32 s37, v249, 38
	s_mov_b32 s60, 0
	s_cmpk_lt_u32 s78, 0xf0
	s_cbranch_scc1 .Lcv_win_B2
	s_cmpk_lt_u32 s78, 0x170
	s_cbranch_scc1 .Lcv_wout_B2
	s_cmpk_lt_u32 s78, 0x970
	s_cbranch_scc1 .Lcv_gu_B2
	s_sub_u32 s78, s78, 0x970
	s_lshr_b32 s83, s78, 6
	s_bfe_u32 s93, s78, 0x30003
	s_and_b32 s94, s78, 7
	s_mul_i32 s98, s77, 0x8000000
	s_lshl_b32 s95, s83, 23
	s_add_u32 s98, s98, s95
	s_lshl_b32 s95, s93, 20
	s_add_u32 s98, s98, s95
	s_lshl_b32 s95, s94, 10
	s_add_u32 s98, s98, s95
	s_mul_i32 s99, s77, 0x4000000
	s_add_u32 s99, s99, 0x14400000
	s_lshl_b32 s95, s83, 22
	s_add_u32 s99, s99, s95
	s_lshl_b32 s95, s94, 19
	s_add_u32 s99, s99, s95
	s_lshl_b32 s95, s93, 8
	s_add_u32 s99, s99, s95
	v_readlane_b32 s30, v249, 4
	v_readlane_b32 s31, v249, 5
	s_movk_i32 s56, 0x2000
	s_movk_i32 s57, 0x800
	s_mov_b32 s59, 0x40000
	s_branch .Lcv_fin_B2
.Lcv_gu_B2:
	s_sub_u32 s78, s78, 0x170
	s_lshr_b32 s83, s78, 10
	s_bfe_u32 s93, s78, 0x40006
	s_bfe_u32 s94, s78, 0x40002
	s_and_b32 s95, s78, 3
	s_mul_i32 s98, s77, 0x8000000
	s_lshl_b32 s78, s93, 23
	s_add_u32 s98, s98, s78
	s_mov_b32 s99, s98
	s_lshl_b32 s78, s94, 19
	s_add_u32 s98, s98, s78
	s_lshl_b32 s78, s95, 10
	s_add_u32 s98, s98, s78
	s_add_u32 s99, s99, 0x4400000
	s_lshl_b32 s78, s95, 21
	s_add_u32 s99, s99, s78
	s_lshl_b32 s78, s83, 19
	s_add_u32 s99, s99, s78
	s_lshl_b32 s78, s94, 8
	s_add_u32 s99, s99, s78
	s_cmp_eq_u32 s83, 0
	s_cbranch_scc0 .Lcv_up_B2
	v_readlane_b32 s30, v249, 0
	v_readlane_b32 s31, v249, 1
	s_branch .Lcv_gu2_B2
.Lcv_up_B2:
	v_readlane_b32 s30, v249, 2
	v_readlane_b32 s31, v249, 3
.Lcv_gu2_B2:
	s_movk_i32 s56, 0x1000
	s_movk_i32 s57, 0x1000
	s_mov_b32 s59, 0x100000
	s_branch .Lcv_fin_B2
.Lcv_wout_B2:
	s_sub_u32 s78, s78, 0xf0
	s_lshr_b32 s83, s78, 3
	s_and_b32 s93, s78, 7
	s_lshl_b32 s98, s77, 24
	s_lshl_b32 s95, s83, 20
	s_add_u32 s98, s98, s95
	s_lshl_b32 s95, s93, 10
	s_add_u32 s98, s98, s95
	s_lshl_b32 s99, s77, 23
	s_add_u32 s99, s99, 0x3400000
	s_lshl_b32 s95, s93, 20
	s_add_u32 s99, s99, s95
	s_lshl_b32 s95, s83, 8
	s_add_u32 s99, s99, s95
	s_lshl_b32 s94, s77, 13
	s_lshl_b32 s95, s83, 9
	s_add_u32 s94, s94, s95
	s_nop 3
	s_add_u32 s36, s36, s94
	s_addc_u32 s37, s37, 0
	v_readlane_b32 s30, v249, 39
	v_readlane_b32 s31, v249, 40
	s_movk_i32 s56, 0x2000
	s_movk_i32 s57, 0x1000
	s_mov_b32 s59, 0x80000
	s_mov_b32 s60, 1
	s_branch .Lcv_fin_B2

; #define PW_SYNC do { asm volatile("s_waitcnt lgkmcnt(0)" ::: "memory"); __builtin_amdgcn_s_barrier(); asm volatile("" ::: "memory"); } while (0)
; __device__ __forceinline__ void ph_weights(const Params& p, LAS unsigned char* lds, const int p0, const int p1, const int wi, const int wn) {
;     ...
;     int pi = p0 + wi; bool hA, hB;
;     PW_LOAD(pi, dA0, dA1, a0, a1, hA);
;     PW_LOAD(pi + wn, dB0, dB1, b0, b1, hB);
;     while (hA) {
;         { PW_TOLDS(dA0, a0, a1); PW_SYNC; const TDesc s0 = dA0, s1 = dA1; PW_LOAD(pi + 2 * wn, dA0, dA1, a0, a1, hA); PW_STORE(s0, s1); PW_SYNC; }
;         if (!hB) break;
;         { PW_TOLDS(dB0, b0, b1); PW_SYNC; const TDesc s0 = dB0, s1 = dB1; PW_LOAD(pi + 3 * wn, dB0, dB1, b0, b1, hB); PW_STORE(s0, s1); PW_SYNC; }
;         pi += 2 * wn;
.Lcv_win3_B2:
	s_lshl_b32 s95, s83, 8
	s_add_u32 s99, s99, s95
	v_readlane_b32 s30, v249, 24
	v_readlane_b32 s31, v249, 25
	s_movk_i32 s56, 0x3c00
	s_movk_i32 s57, 0x1000
	s_mov_b32 s59, 0x80000
.Lcv_fin_B2:
	s_nop 3
	s_add_u32 s30, s30, s98
	s_addc_u32 s31, s31, 0
	s_add_u32 s32, s26, s99
	s_addc_u32 s33, s27, 0
	v_mad_u32_u24 v177, v168, s56, v169
	s_mov_b64 s[88:89], s[30:31]
	s_add_u32 s90, s30, s56
	s_addc_u32 s91, s31, 0
	s_lshl_b32 s92, s56, 5
	global_load_dwordx2 v[146:147], v170, s[36:37]
	global_load_dwordx2 v[148:149], v170, s[36:37] offset:128
	global_load_dwordx2 v[150:151], v170, s[36:37] offset:256
	global_load_dwordx2 v[152:153], v170, s[36:37] offset:384
	global_load_dwordx4 v[66:69], v177, s[88:89] nt
	global_load_dwordx4 v[98:101], v177, s[88:89] offset:512 nt
	global_load_dwordx4 v[70:73], v177, s[90:91] nt
	global_load_dwordx4 v[102:105], v177, s[90:91] offset:512 nt
	s_add_u32 s88, s88, s92
	s_addc_u32 s89, s89, 0
	s_add_u32 s90, s90, s92
	s_addc_u32 s91, s91, 0
	global_load_dwordx4 v[74:77], v177, s[88:89] nt
	global_load_dwordx4 v[106:109], v177, s[88:89] offset:512 nt
	global_load_dwordx4 v[78:81], v177, s[90:91] nt
	global_load_dwordx4 v[110:113], v177, s[90:91] offset:512 nt
	s_add_u32 s88, s88, s92
	s_addc_u32 s89, s89, 0
	s_add_u32 s90, s90, s92
	s_addc_u32 s91, s91, 0
	global_load_dwordx4 v[82:85], v177, s[88:89] nt
	global_load_dwordx4 v[114:117], v177, s[88:89] offset:512 nt
	global_load_dwordx4 v[86:89], v177, s[90:91] nt
	global_load_dwordx4 v[118:121], v177, s[90:91] offset:512 nt
	s_add_u32 s88, s88, s92
	s_addc_u32 s89, s89, 0
	s_add_u32 s90, s90, s92
	s_addc_u32 s91, s91, 0
	global_load_dwordx4 v[90:93], v177, s[88:89] nt
	global_load_dwordx4 v[122:125], v177, s[88:89] offset:512 nt
	global_load_dwordx4 v[94:97], v177, s[90:91] nt
	global_load_dwordx4 v[126:129], v177, s[90:91] offset:512 nt
	global_load_dword v1, v170, s[36:37]
	global_load_dword v1, v170, s[36:37]
	global_load_dword v1, v170, s[36:37]
	global_load_dword v1, v170, s[36:37]
	global_load_dword v1, v170, s[36:37]
	global_load_dword v1, v170, s[36:37]
	global_load_dword v1, v170, s[36:37]
	global_load_dword v1, v170, s[36:37]
.Lcv_loop:
	s_and_b32 s8, s9, 1
	s_cmp_eq_u32 s8, 0
	s_cbranch_scc1 .Lcv_done
	s_mov_b64 s[84:85], s[14:15]
	s_mov_b32 s69, s23
	s_mov_b32 s75, s28
	s_mov_b32 s87, s29
	s_add_u32 s86, s0, 192
	s_cmp_lt_u32 s86, 0x1ae0
	s_cbranch_scc1 .Lcv_dec_A
	s_andn2_b32 s9, s9, 1
	s_branch .Lcv_ld_A
.Lcv_dec_A:
	s_cmp_ge_u32 s86, 0xd70
	s_cselect_b32 s77, 1, 0
	s_mul_i32 s83, s77, 0xd70
	s_sub_u32 s78, s86, s83
	v_readlane_b32 s20, v249, 37
	v_readlane_b32 s21, v249, 38
	s_mov_b32 s29, 0
	s_cmpk_lt_u32 s78, 0xf0
	s_cbranch_scc1 .Lcv_win_A3
	s_cmpk_lt_u32 s78, 0x170
	s_cbranch_scc1 .Lcv_wout_A3
	s_cmpk_lt_u32 s78, 0x970
	s_cbranch_scc1 .Lcv_gu_A3
	s_sub_u32 s78, s78, 0x970
	s_lshr_b32 s83, s78, 6
	s_bfe_u32 s93, s78, 0x30003
	s_and_b32 s94, s78, 7
	s_mul_i32 s98, s77, 0x8000000
	s_lshl_b32 s95, s83, 23
	s_add_u32 s98, s98, s95
	s_lshl_b32 s95, s93, 20
	s_add_u32 s98, s98, s95
	s_lshl_b32 s95, s94, 10
	s_add_u32 s98, s98, s95
	s_mul_i32 s99, s77, 0x4000000
	s_add_u32 s99, s99, 0x14400000
	s_lshl_b32 s95, s83, 22
	s_add_u32 s99, s99, s95
	s_lshl_b32 s95, s94, 19
	s_add_u32 s99, s99, s95
	s_lshl_b32 s95, s93, 8
	s_add_u32 s99, s99, s95
	v_readlane_b32 s12, v249, 4
	v_readlane_b32 s13, v249, 5
	s_movk_i32 s22, 0x2000
	s_movk_i32 s23, 0x800
	s_mov_b32 s28, 0x40000
	s_branch .Lcv_fin_A3

.Lcv_fin_A3:
	s_nop 3
	s_add_u32 s12, s12, s98
	s_addc_u32 s13, s13, 0
	s_add_u32 s14, s26, s99
	s_addc_u32 s15, s27, 0
.Lcv_ld_A:
	s_waitcnt vmcnt(44)
	s_cmp_eq_u32 s87, 0
	s_cbranch_scc1 .Lcv_nosc0_At
	v_mul_f32_e32 v2, v138, v2
	v_mul_f32_e32 v3, v138, v3
	v_mul_f32_e32 v4, v138, v4
	v_mul_f32_e32 v5, v138, v5
	v_mul_f32_e32 v34, v138, v34
	v_mul_f32_e32 v35, v138, v35
	v_mul_f32_e32 v36, v138, v36
	v_mul_f32_e32 v37, v138, v37
	v_mul_f32_e32 v6, v139, v6
	v_mul_f32_e32 v7, v139, v7
	v_mul_f32_e32 v8, v139, v8
	v_mul_f32_e32 v9, v139, v9
	v_mul_f32_e32 v38, v139, v38
	v_mul_f32_e32 v39, v139, v39
	v_mul_f32_e32 v40, v139, v40
	v_mul_f32_e32 v41, v139, v41
	v_mul_f32_e32 v10, v140, v10
	v_mul_f32_e32 v11, v140, v11
	v_mul_f32_e32 v12, v140, v12
	v_mul_f32_e32 v13, v140, v13
	v_mul_f32_e32 v42, v140, v42
	v_mul_f32_e32 v43, v140, v43
	v_mul_f32_e32 v44, v140, v44
	v_mul_f32_e32 v45, v140, v45
	v_mul_f32_e32 v14, v141, v14
	v_mul_f32_e32 v15, v141, v15
	v_mul_f32_e32 v16, v141, v16
	v_mul_f32_e32 v17, v141, v17
	v_mul_f32_e32 v46, v141, v46
	v_mul_f32_e32 v47, v141, v47
	v_mul_f32_e32 v48, v141, v48
	v_mul_f32_e32 v49, v141, v49
.Lcv_nosc0_At:
	v_cvt_pk_bf16_f32 v2, v2, v6
	v_cvt_pk_bf16_f32 v3, v3, v7
	v_cvt_pk_bf16_f32 v4, v4, v8
	v_cvt_pk_bf16_f32 v5, v5, v9
	v_cvt_pk_bf16_f32 v34, v34, v38
	v_cvt_pk_bf16_f32 v35, v35, v39
	v_cvt_pk_bf16_f32 v36, v36, v40
	v_cvt_pk_bf16_f32 v37, v37, v41
	ds_write_b128 v154, v[2:5]
	ds_write_b128 v154, v[34:37] offset:32768
	v_cvt_pk_bf16_f32 v10, v10, v14
	v_cvt_pk_bf16_f32 v11, v11, v15
	v_cvt_pk_bf16_f32 v12, v12, v16
	v_cvt_pk_bf16_f32 v13, v13, v17
	v_cvt_pk_bf16_f32 v42, v42, v46
	v_cvt_pk_bf16_f32 v43, v43, v47
	v_cvt_pk_bf16_f32 v44, v44, v48
	v_cvt_pk_bf16_f32 v45, v45, v49
	ds_write_b128 v155, v[10:13] offset:8192
	ds_write_b128 v155, v[42:45] offset:40960
	s_waitcnt vmcnt(36)
	s_cmp_eq_u32 s87, 0
	s_cbranch_scc1 .Lcv_nosc1_At
	v_mul_f32_e32 v18, v142, v18
	v_mul_f32_e32 v19, v142, v19
	v_mul_f32_e32 v20, v142, v20
	v_mul_f32_e32 v21, v142, v21
	v_mul_f32_e32 v50, v142, v50
	v_mul_f32_e32 v51, v142, v51
	v_mul_f32_e32 v52, v142, v52
	v_mul_f32_e32 v53, v142, v53
	v_mul_f32_e32 v22, v143, v22
	v_mul_f32_e32 v23, v143, v23
	v_mul_f32_e32 v24, v143, v24
	v_mul_f32_e32 v25, v143, v25
	v_mul_f32_e32 v54, v143, v54
	v_mul_f32_e32 v55, v143, v55
	v_mul_f32_e32 v56, v143, v56
	v_mul_f32_e32 v57, v143, v57
	v_mul_f32_e32 v26, v144, v26
	v_mul_f32_e32 v27, v144, v27
	v_mul_f32_e32 v28, v144, v28
	v_mul_f32_e32 v29, v144, v29
	v_mul_f32_e32 v58, v144, v58
	v_mul_f32_e32 v59, v144, v59
	v_mul_f32_e32 v60, v144, v60
	v_mul_f32_e32 v61, v144, v61
	v_mul_f32_e32 v30, v145, v30
	v_mul_f32_e32 v31, v145, v31
	v_mul_f32_e32 v32, v145, v32
	v_mul_f32_e32 v33, v145, v33
	v_mul_f32_e32 v62, v145, v62
	v_mul_f32_e32 v63, v145, v63
	v_mul_f32_e32 v64, v145, v64
	v_mul_f32_e32 v65, v145, v65
; #define PW_SYNC do { asm volatile("s_waitcnt lgkmcnt(0)" ::: "memory"); __builtin_amdgcn_s_barrier(); asm volatile("" ::: "memory"); } while (0)
; __device__ __forceinline__ void ph_weights(const Params& p, LAS unsigned char* lds, const int p0, const int p1, const int wi, const int wn) {
;     ...
;     int pi = p0 + wi; bool hA, hB;
;     PW_LOAD(pi, dA0, dA1, a0, a1, hA);
;     PW_LOAD(pi + wn, dB0, dB1, b0, b1, hB);
;     while (hA) {
;         { PW_TOLDS(dA0, a0, a1); PW_SYNC; const TDesc s0 = dA0, s1 = dA1; PW_LOAD(pi + 2 * wn, dA0, dA1, a0, a1, hA); PW_STORE(s0, s1); PW_SYNC; }
;         if (!hB) break;
;         { PW_TOLDS(dB0, b0, b1); PW_SYNC; const TDesc s0 = dB0, s1 = dB1; PW_LOAD(pi + 3 * wn, dB0, dB1, b0, b1, hB); PW_STORE(s0, s1); PW_SYNC; }
.Lcv_nosc1_At:
	v_cvt_pk_bf16_f32 v18, v18, v22
	v_cvt_pk_bf16_f32 v19, v19, v23
	v_cvt_pk_bf16_f32 v20, v20, v24
	v_cvt_pk_bf16_f32 v21, v21, v25
	v_cvt_pk_bf16_f32 v50, v50, v54
	v_cvt_pk_bf16_f32 v51, v51, v55
	v_cvt_pk_bf16_f32 v52, v52, v56
	v_cvt_pk_bf16_f32 v53, v53, v57
	ds_write_b128 v156, v[18:21] offset:16384
	ds_write_b128 v156, v[50:53] offset:49152
	v_cvt_pk_bf16_f32 v26, v26, v30
	v_cvt_pk_bf16_f32 v27, v27, v31
	v_cvt_pk_bf16_f32 v28, v28, v32
	v_cvt_pk_bf16_f32 v29, v29, v33
	v_cvt_pk_bf16_f32 v58, v58, v62
	v_cvt_pk_bf16_f32 v59, v59, v63
	v_cvt_pk_bf16_f32 v60, v60, v64
	v_cvt_pk_bf16_f32 v61, v61, v65
	ds_write_b128 v157, v[26:29] offset:24576
	ds_write_b128 v157, v[58:61] offset:57344
	v_mad_u32_u24 v177, v168, s22, v169
	s_mov_b64 s[88:89], s[12:13]
	s_add_u32 s90, s12, s22
	s_addc_u32 s91, s13, 0
	s_lshl_b32 s92, s22, 5
	global_load_dwordx2 v[138:139], v170, s[20:21]
	global_load_dwordx2 v[140:141], v170, s[20:21] offset:128
	global_load_dwordx2 v[142:143], v170, s[20:21] offset:256
	global_load_dwordx2 v[144:145], v170, s[20:21] offset:384
	global_load_dwordx4 v[2:5], v177, s[88:89] nt
	global_load_dwordx4 v[34:37], v177, s[88:89] offset:512 nt
	global_load_dwordx4 v[6:9], v177, s[90:91] nt
	global_load_dwordx4 v[38:41], v177, s[90:91] offset:512 nt
	s_add_u32 s88, s88, s92
	s_addc_u32 s89, s89, 0
	s_add_u32 s90, s90, s92
	s_addc_u32 s91, s91, 0
	global_load_dwordx4 v[10:13], v177, s[88:89] nt
	global_load_dwordx4 v[42:45], v177, s[88:89] offset:512 nt
	global_load_dwordx4 v[14:17], v177, s[90:91] nt
	global_load_dwordx4 v[46:49], v177, s[90:91] offset:512 nt
	s_add_u32 s88, s88, s92
	s_addc_u32 s89, s89, 0
	s_add_u32 s90, s90, s92
	s_addc_u32 s91, s91, 0
	global_load_dwordx4 v[18:21], v177, s[88:89] nt
	global_load_dwordx4 v[50:53], v177, s[88:89] offset:512 nt
	global_load_dwordx4 v[22:25], v177, s[90:91] nt
	global_load_dwordx4 v[54:57], v177, s[90:91] offset:512 nt
	s_add_u32 s88, s88, s92
	s_addc_u32 s89, s89, 0
	s_add_u32 s90, s90, s92
	s_addc_u32 s91, s91, 0
	global_load_dwordx4 v[26:29], v177, s[88:89] nt
	global_load_dwordx4 v[58:61], v177, s[88:89] offset:512 nt
	global_load_dwordx4 v[30:33], v177, s[90:91] nt
	global_load_dwordx4 v[62:65], v177, s[90:91] offset:512 nt
	s_waitcnt lgkmcnt(0)
	s_barrier
	v_mad_u32_u24 v178, v175, s69, v176
	s_mov_b64 s[88:89], s[84:85]
	s_add_u32 s90, s84, s75
	s_addc_u32 s91, s85, 0
	s_lshl_b32 s92, s69, 5
	ds_read_b32 v228, v162
	ds_read_b32 v229, v162 offset:512
	ds_read_b32 v230, v162 offset:1024
	ds_read_b32 v231, v162 offset:1536
	ds_read_b32 v232, v162 offset:32768
	ds_read_b32 v233, v162 offset:33280
	ds_read_b32 v234, v162 offset:33792
	ds_read_b32 v235, v162 offset:34304
	s_waitcnt lgkmcnt(0)
	ds_read_b32 v204, v163
	ds_read_b32 v205, v163 offset:512
	ds_read_b32 v206, v163 offset:1024
	ds_read_b32 v207, v163 offset:1536
	ds_read_b32 v208, v163 offset:32768
	ds_read_b32 v209, v163 offset:33280
	ds_read_b32 v210, v163 offset:33792
	ds_read_b32 v211, v163 offset:34304
	global_store_dwordx4 v178, v[228:231], s[88:89] nt
	global_store_dwordx4 v178, v[232:235], s[90:91] nt
	s_add_u32 s88, s88, s92
	s_addc_u32 s89, s89, 0
	s_add_u32 s90, s90, s92
	s_addc_u32 s91, s91, 0
	s_waitcnt lgkmcnt(0)
	ds_read_b32 v228, v164
	ds_read_b32 v229, v164 offset:512
	ds_read_b32 v230, v164 offset:1024
	ds_read_b32 v231, v164 offset:1536
	ds_read_b32 v232, v164 offset:32768
	ds_read_b32 v233, v164 offset:33280
	ds_read_b32 v234, v164 offset:33792
	ds_read_b32 v235, v164 offset:34304
	global_store_dwordx4 v178, v[204:207], s[88:89] nt
	global_store_dwordx4 v178, v[208:211], s[90:91] nt
	s_add_u32 s88, s88, s92
	s_addc_u32 s89, s89, 0
	s_add_u32 s90, s90, s92
	s_addc_u32 s91, s91, 0
	s_waitcnt lgkmcnt(0)
	ds_read_b32 v204, v165
	ds_read_b32 v205, v165 offset:512
	ds_read_b32 v206, v165 offset:1024
	ds_read_b32 v207, v165 offset:1536
	ds_read_b32 v208, v165 offset:32768
	ds_read_b32 v209, v165 offset:33280
	ds_read_b32 v210, v165 offset:33792
	ds_read_b32 v211, v165 offset:34304
	global_store_dwordx4 v178, v[228:231], s[88:89] nt
	global_store_dwordx4 v178, v[232:235], s[90:91] nt
	s_add_u32 s88, s88, s92
	s_addc_u32 s89, s89, 0
	s_add_u32 s90, s90, s92
	s_addc_u32 s91, s91, 0
	s_waitcnt lgkmcnt(0)
	global_store_dwordx4 v178, v[204:207], s[88:89] nt
	global_store_dwordx4 v178, v[208:211], s[90:91] nt
	s_and_b32 s8, s9, 2
	s_cmp_eq_u32 s8, 0
	s_cbranch_scc1 .Lcv_done
	s_mov_b64 s[84:85], s[32:33]
	s_mov_b32 s69, s57
	s_mov_b32 s75, s59
	s_mov_b32 s87, s60
	s_add_u32 s86, s0, 288
	s_cmp_lt_u32 s86, 0x1ae0
	s_cbranch_scc1 .Lcv_dec_B
	s_andn2_b32 s9, s9, 2
	s_branch .Lcv_ld_B
.Lcv_dec_B:
	s_cmp_ge_u32 s86, 0xd70
	s_cselect_b32 s77, 1, 0
	s_mul_i32 s83, s77, 0xd70
	s_sub_u32 s78, s86, s83
	v_readlane_b32 s36, v249, 37
	v_readlane_b32 s37, v249, 38
	s_mov_b32 s60, 0
	s_cmpk_lt_u32 s78, 0xf0
	s_cbranch_scc1 .Lcv_win_B4
	s_cmpk_lt_u32 s78, 0x170
	s_cbranch_scc1 .Lcv_wout_B4
	s_cmpk_lt_u32 s78, 0x970
	s_cbranch_scc1 .Lcv_gu_B4
	s_sub_u32 s78, s78, 0x970
	s_lshr_b32 s83, s78, 6
	s_bfe_u32 s93, s78, 0x30003
	s_and_b32 s94, s78, 7
	s_mul_i32 s98, s77, 0x8000000
	s_lshl_b32 s95, s83, 23
	s_add_u32 s98, s98, s95
	s_lshl_b32 s95, s93, 20
	s_add_u32 s98, s98, s95
	s_lshl_b32 s95, s94, 10
	s_add_u32 s98, s98, s95
	s_mul_i32 s99, s77, 0x4000000
	s_add_u32 s99, s99, 0x14400000
	s_lshl_b32 s95, s83, 22
	s_add_u32 s99, s99, s95
	s_lshl_b32 s95, s94, 19
	s_add_u32 s99, s99, s95
	s_lshl_b32 s95, s93, 8
	s_add_u32 s99, s99, s95
	v_readlane_b32 s30, v249, 4
	v_readlane_b32 s31, v249, 5
	s_movk_i32 s56, 0x2000
	s_movk_i32 s57, 0x800
	s_mov_b32 s59, 0x40000
	s_branch .Lcv_fin_B4

; #define PW_SYNC do { asm volatile("s_waitcnt lgkmcnt(0)" ::: "memory"); __builtin_amdgcn_s_barrier(); asm volatile("" ::: "memory"); } while (0)
; __device__ __forceinline__ void ph_weights(const Params& p, LAS unsigned char* lds, const int p0, const int p1, const int wi, const int wn) {
;     ...
;         { PW_TOLDS(dB0, b0, b1); PW_SYNC; const TDesc s0 = dB0, s1 = dB1; PW_LOAD(pi + 3 * wn, dB0, dB1, b0, b1, hB); PW_STORE(s0, s1); PW_SYNC; }
.Lcv_fin_B4:
	s_nop 3
	s_add_u32 s30, s30, s98
	s_addc_u32 s31, s31, 0
	s_add_u32 s32, s26, s99
	s_addc_u32 s33, s27, 0
.Lcv_ld_B:
	s_waitcnt vmcnt(44)
	s_cmp_eq_u32 s87, 0
	s_cbranch_scc1 .Lcv_nosc0_Bt
	v_mul_f32_e32 v66, v146, v66
	v_mul_f32_e32 v67, v146, v67
	v_mul_f32_e32 v68, v146, v68
	v_mul_f32_e32 v69, v146, v69
	v_mul_f32_e32 v98, v146, v98
	v_mul_f32_e32 v99, v146, v99
	v_mul_f32_e32 v100, v146, v100
	v_mul_f32_e32 v101, v146, v101
	v_mul_f32_e32 v70, v147, v70
	v_mul_f32_e32 v71, v147, v71
	v_mul_f32_e32 v72, v147, v72
	v_mul_f32_e32 v73, v147, v73
	v_mul_f32_e32 v102, v147, v102
	v_mul_f32_e32 v103, v147, v103
	v_mul_f32_e32 v104, v147, v104
	v_mul_f32_e32 v105, v147, v105
	v_mul_f32_e32 v74, v148, v74
	v_mul_f32_e32 v75, v148, v75
	v_mul_f32_e32 v76, v148, v76
	v_mul_f32_e32 v77, v148, v77
	v_mul_f32_e32 v106, v148, v106
	v_mul_f32_e32 v107, v148, v107
	v_mul_f32_e32 v108, v148, v108
	v_mul_f32_e32 v109, v148, v109
	v_mul_f32_e32 v78, v149, v78
	v_mul_f32_e32 v79, v149, v79
	v_mul_f32_e32 v80, v149, v80
	v_mul_f32_e32 v81, v149, v81
	v_mul_f32_e32 v110, v149, v110
	v_mul_f32_e32 v111, v149, v111
	v_mul_f32_e32 v112, v149, v112
	v_mul_f32_e32 v113, v149, v113
.Lcv_nosc0_Bt:
	v_cvt_pk_bf16_f32 v66, v66, v70
	v_cvt_pk_bf16_f32 v67, v67, v71
	v_cvt_pk_bf16_f32 v68, v68, v72
	v_cvt_pk_bf16_f32 v69, v69, v73
	v_cvt_pk_bf16_f32 v98, v98, v102
	v_cvt_pk_bf16_f32 v99, v99, v103
	v_cvt_pk_bf16_f32 v100, v100, v104
	v_cvt_pk_bf16_f32 v101, v101, v105
	ds_write_b128 v158, v[66:69]
	ds_write_b128 v158, v[98:101] offset:32768
	v_cvt_pk_bf16_f32 v74, v74, v78
	v_cvt_pk_bf16_f32 v75, v75, v79
	v_cvt_pk_bf16_f32 v76, v76, v80
	v_cvt_pk_bf16_f32 v77, v77, v81
	v_cvt_pk_bf16_f32 v106, v106, v110
	v_cvt_pk_bf16_f32 v107, v107, v111
	v_cvt_pk_bf16_f32 v108, v108, v112
	v_cvt_pk_bf16_f32 v109, v109, v113
	ds_write_b128 v159, v[74:77] offset:8192
	ds_write_b128 v159, v[106:109] offset:40960
	s_waitcnt vmcnt(36)
	s_cmp_eq_u32 s87, 0
	s_cbranch_scc1 .Lcv_nosc1_Bt
	v_mul_f32_e32 v82, v150, v82
	v_mul_f32_e32 v83, v150, v83
	v_mul_f32_e32 v84, v150, v84
	v_mul_f32_e32 v85, v150, v85
	v_mul_f32_e32 v114, v150, v114
	v_mul_f32_e32 v115, v150, v115
	v_mul_f32_e32 v116, v150, v116
	v_mul_f32_e32 v117, v150, v117
	v_mul_f32_e32 v86, v151, v86
	v_mul_f32_e32 v87, v151, v87
	v_mul_f32_e32 v88, v151, v88
	v_mul_f32_e32 v89, v151, v89
	v_mul_f32_e32 v118, v151, v118
	v_mul_f32_e32 v119, v151, v119
	v_mul_f32_e32 v120, v151, v120
	v_mul_f32_e32 v121, v151, v121
	v_mul_f32_e32 v90, v152, v90
	v_mul_f32_e32 v91, v152, v91
	v_mul_f32_e32 v92, v152, v92
	v_mul_f32_e32 v93, v152, v93
	v_mul_f32_e32 v122, v152, v122
	v_mul_f32_e32 v123, v152, v123
	v_mul_f32_e32 v124, v152, v124
	v_mul_f32_e32 v125, v152, v125
	v_mul_f32_e32 v94, v153, v94
	v_mul_f32_e32 v95, v153, v95
	v_mul_f32_e32 v96, v153, v96
	v_mul_f32_e32 v97, v153, v97
	v_mul_f32_e32 v126, v153, v126
	v_mul_f32_e32 v127, v153, v127
	v_mul_f32_e32 v128, v153, v128
	v_mul_f32_e32 v129, v153, v129
; #define PW_SYNC do { asm volatile("s_waitcnt lgkmcnt(0)" ::: "memory"); __builtin_amdgcn_s_barrier(); asm volatile("" ::: "memory"); } while (0)
; __device__ __forceinline__ void ph_weights(const Params& p, LAS unsigned char* lds, const int p0, const int p1, const int wi, const int wn) {
;     ...
;     int pi = p0 + wi; bool hA, hB;
;     PW_LOAD(pi, dA0, dA1, a0, a1, hA);
;     PW_LOAD(pi + wn, dB0, dB1, b0, b1, hB);
;     while (hA) {
;         { PW_TOLDS(dA0, a0, a1); PW_SYNC; const TDesc s0 = dA0, s1 = dA1; PW_LOAD(pi + 2 * wn, dA0, dA1, a0, a1, hA); PW_STORE(s0, s1); PW_SYNC; }
;         if (!hB) break;
;         { PW_TOLDS(dB0, b0, b1); PW_SYNC; const TDesc s0 = dB0, s1 = dB1; PW_LOAD(pi + 3 * wn, dB0, dB1, b0, b1, hB); PW_STORE(s0, s1); PW_SYNC; }
;         pi += 2 * wn;
;     }
.Lcv_nosc1_Bt:
	v_cvt_pk_bf16_f32 v82, v82, v86
	v_cvt_pk_bf16_f32 v83, v83, v87
	v_cvt_pk_bf16_f32 v84, v84, v88
	v_cvt_pk_bf16_f32 v85, v85, v89
	v_cvt_pk_bf16_f32 v114, v114, v118
	v_cvt_pk_bf16_f32 v115, v115, v119
	v_cvt_pk_bf16_f32 v116, v116, v120
	v_cvt_pk_bf16_f32 v117, v117, v121
	ds_write_b128 v160, v[82:85] offset:16384
	ds_write_b128 v160, v[114:117] offset:49152
	v_cvt_pk_bf16_f32 v90, v90, v94
	v_cvt_pk_bf16_f32 v91, v91, v95
	v_cvt_pk_bf16_f32 v92, v92, v96
	v_cvt_pk_bf16_f32 v93, v93, v97
	v_cvt_pk_bf16_f32 v122, v122, v126
	v_cvt_pk_bf16_f32 v123, v123, v127
	v_cvt_pk_bf16_f32 v124, v124, v128
	v_cvt_pk_bf16_f32 v125, v125, v129
	ds_write_b128 v161, v[90:93] offset:24576
	ds_write_b128 v161, v[122:125] offset:57344
	v_mad_u32_u24 v177, v168, s56, v169
	s_mov_b64 s[88:89], s[30:31]
	s_add_u32 s90, s30, s56
	s_addc_u32 s91, s31, 0
	s_lshl_b32 s92, s56, 5
	global_load_dwordx2 v[146:147], v170, s[36:37]
	global_load_dwordx2 v[148:149], v170, s[36:37] offset:128
	global_load_dwordx2 v[150:151], v170, s[36:37] offset:256
	global_load_dwordx2 v[152:153], v170, s[36:37] offset:384
	global_load_dwordx4 v[66:69], v177, s[88:89] nt
	global_load_dwordx4 v[98:101], v177, s[88:89] offset:512 nt
	global_load_dwordx4 v[70:73], v177, s[90:91] nt
	global_load_dwordx4 v[102:105], v177, s[90:91] offset:512 nt
	s_add_u32 s88, s88, s92
	s_addc_u32 s89, s89, 0
	s_add_u32 s90, s90, s92
	s_addc_u32 s91, s91, 0
	global_load_dwordx4 v[74:77], v177, s[88:89] nt
	global_load_dwordx4 v[106:109], v177, s[88:89] offset:512 nt
	global_load_dwordx4 v[78:81], v177, s[90:91] nt
	global_load_dwordx4 v[110:113], v177, s[90:91] offset:512 nt
	s_add_u32 s88, s88, s92
	s_addc_u32 s89, s89, 0
	s_add_u32 s90, s90, s92
	s_addc_u32 s91, s91, 0
	global_load_dwordx4 v[82:85], v177, s[88:89] nt
	global_load_dwordx4 v[114:117], v177, s[88:89] offset:512 nt
	global_load_dwordx4 v[86:89], v177, s[90:91] nt
	global_load_dwordx4 v[118:121], v177, s[90:91] offset:512 nt
	s_add_u32 s88, s88, s92
	s_addc_u32 s89, s89, 0
	s_add_u32 s90, s90, s92
	s_addc_u32 s91, s91, 0
	global_load_dwordx4 v[90:93], v177, s[88:89] nt
	global_load_dwordx4 v[122:125], v177, s[88:89] offset:512 nt
	global_load_dwordx4 v[94:97], v177, s[90:91] nt
	global_load_dwordx4 v[126:129], v177, s[90:91] offset:512 nt
	s_waitcnt lgkmcnt(0)
	s_barrier
	v_mad_u32_u24 v178, v175, s69, v176
	s_mov_b64 s[88:89], s[84:85]
	s_add_u32 s90, s84, s75
	s_addc_u32 s91, s85, 0
	s_lshl_b32 s92, s69, 5
	ds_read_b32 v228, v130
	ds_read_b32 v229, v130 offset:512
	ds_read_b32 v230, v130 offset:1024
	ds_read_b32 v231, v130 offset:1536
	ds_read_b32 v232, v130 offset:32768
	ds_read_b32 v233, v130 offset:33280
	ds_read_b32 v234, v130 offset:33792
	ds_read_b32 v235, v130 offset:34304
	s_waitcnt lgkmcnt(0)
	ds_read_b32 v204, v131
	ds_read_b32 v205, v131 offset:512
	ds_read_b32 v206, v131 offset:1024
	ds_read_b32 v207, v131 offset:1536
	ds_read_b32 v208, v131 offset:32768
	ds_read_b32 v209, v131 offset:33280
	ds_read_b32 v210, v131 offset:33792
	ds_read_b32 v211, v131 offset:34304
	global_store_dwordx4 v178, v[228:231], s[88:89] nt
	global_store_dwordx4 v178, v[232:235], s[90:91] nt
	s_add_u32 s88, s88, s92
	s_addc_u32 s89, s89, 0
	s_add_u32 s90, s90, s92
	s_addc_u32 s91, s91, 0
	s_waitcnt lgkmcnt(0)
	ds_read_b32 v228, v132
	ds_read_b32 v229, v132 offset:512
	ds_read_b32 v230, v132 offset:1024
	ds_read_b32 v231, v132 offset:1536
	ds_read_b32 v232, v132 offset:32768
	ds_read_b32 v233, v132 offset:33280
	ds_read_b32 v234, v132 offset:33792
	ds_read_b32 v235, v132 offset:34304
	global_store_dwordx4 v178, v[204:207], s[88:89] nt
	global_store_dwordx4 v178, v[208:211], s[90:91] nt
	s_add_u32 s88, s88, s92
	s_addc_u32 s89, s89, 0
	s_add_u32 s90, s90, s92
	s_addc_u32 s91, s91, 0
	s_waitcnt lgkmcnt(0)
	ds_read_b32 v204, v133
	ds_read_b32 v205, v133 offset:512
	ds_read_b32 v206, v133 offset:1024
	ds_read_b32 v207, v133 offset:1536
	ds_read_b32 v208, v133 offset:32768
	ds_read_b32 v209, v133 offset:33280
	ds_read_b32 v210, v133 offset:33792
	ds_read_b32 v211, v133 offset:34304
	global_store_dwordx4 v178, v[228:231], s[88:89] nt
	global_store_dwordx4 v178, v[232:235], s[90:91] nt
	s_add_u32 s88, s88, s92
	s_addc_u32 s89, s89, 0
	s_add_u32 s90, s90, s92
	s_addc_u32 s91, s91, 0
	s_waitcnt lgkmcnt(0)
	global_store_dwordx4 v178, v[204:207], s[88:89] nt
	global_store_dwordx4 v178, v[208:211], s[90:91] nt
	s_add_u32 s0, s0, 192
	s_branch .Lcv_loop
.Lcv_done:
	s_waitcnt vmcnt(0)
	s_branch .LBB0_902
